# peeled first K iteration with SrcC=0 MFMAs: no accumulator zeroing at 5 GEMM sites (plus K-swizzle)
# speedup vs baseline: 1.2475x; 1.0009x over previous
.LBB0_809:
	s_andn2_b64 vcc, exec, s[52:53]
	s_waitcnt vmcnt(0)
	s_cbranch_vccnz .LBB0_812
	s_add_u32 s26, s26, 0x80
	s_addc_u32 s27, s27, 0
	s_add_u32 s19, s30, 0x100
	s_addc_u32 s20, s31, 0
	s_mov_b32 s21, 0
	s_add_i32 s22, s21, 2
	s_add_u32 s23, s26, 0x80
	s_addc_u32 s28, s27, 0
	s_add_i32 s34, 0, 0x10000
	s_cmp_eq_u32 s81, s21
	s_cselect_b32 s31, s3, s28
	s_cselect_b32 s30, s2, s23
	v_add_u32_e32 v2, s34, v231
	s_cselect_b32 s29, s61, s20
	s_cselect_b32 s28, s60, s19
	s_add_i32 s21, 0, 0x14000
	ds_read_b128 v[100:103], v2
	ds_read_b128 v[104:107], v2 offset:1024
	ds_read_b128 v[108:111], v2 offset:2048
	ds_read_b128 v[112:115], v2 offset:3072
	v_add_u32_e32 v2, s21, v231
	ds_read_b128 v[132:135], v2
	ds_read_b128 v[136:139], v2 offset:1024
	ds_read_b128 v[140:143], v2 offset:2048
	ds_read_b128 v[144:147], v2 offset:3072
	v_lshl_add_u64 v[208:209], s[26:27], 0, v[204:205]
	s_add_i32 m0, s72, 0xc000
	ds_read_b128 v[164:167], v240
	ds_read_b128 v[168:171], v240 offset:1024
	ds_read_b128 v[172:175], v240 offset:2048
	ds_read_b128 v[176:179], v240 offset:3072
	ds_read_b128 v[180:183], v240 offset:4096
	ds_read_b128 v[184:187], v240 offset:5120
	ds_read_b128 v[188:191], v240 offset:6144
	ds_read_b128 v[192:195], v240 offset:7168
	global_load_lds_dwordx4 v[208:209], off
	v_lshl_add_u64 v[208:209], s[26:27], 0, v[206:207]
	s_add_i32 m0, s72, 0xe000
	s_nop 0
	global_load_lds_dwordx4 v[208:209], off
	s_waitcnt vmcnt(8)
	s_waitcnt lgkmcnt(0)
	s_barrier
	s_setprio 1
	s_waitcnt lgkmcnt(0)
	v_mfma_f32_16x16x32_bf16 v[160:163], v[100:103], v[164:167], 0
	v_mfma_f32_16x16x32_bf16 v[156:159], v[108:111], v[164:167], 0
	v_mfma_f32_16x16x32_bf16 v[128:131], v[100:103], v[172:175], 0
	v_mfma_f32_16x16x32_bf16 v[124:127], v[108:111], v[172:175], 0
	v_mfma_f32_16x16x32_bf16 v[96:99], v[100:103], v[180:183], 0
	v_mfma_f32_16x16x32_bf16 v[92:95], v[108:111], v[180:183], 0
	v_mfma_f32_16x16x32_bf16 v[80:83], v[100:103], v[188:191], 0
	v_mfma_f32_16x16x32_bf16 v[76:79], v[108:111], v[188:191], 0
	v_mfma_f32_16x16x32_bf16 v[160:163], v[104:107], v[168:171], v[160:163]
	v_mfma_f32_16x16x32_bf16 v[156:159], v[112:115], v[168:171], v[156:159]
	v_mfma_f32_16x16x32_bf16 v[128:131], v[104:107], v[176:179], v[128:131]
	v_mfma_f32_16x16x32_bf16 v[124:127], v[112:115], v[176:179], v[124:127]
	v_mfma_f32_16x16x32_bf16 v[96:99], v[104:107], v[184:187], v[96:99]
	v_mfma_f32_16x16x32_bf16 v[92:95], v[112:115], v[184:187], v[92:95]
	v_mfma_f32_16x16x32_bf16 v[80:83], v[104:107], v[192:195], v[80:83]
	v_mfma_f32_16x16x32_bf16 v[76:79], v[112:115], v[192:195], v[76:79]
	s_setprio 0
	s_setprio 1
	v_mfma_f32_16x16x32_bf16 v[152:155], v[132:135], v[164:167], 0
	v_mfma_f32_16x16x32_bf16 v[148:151], v[140:143], v[164:167], 0
	v_mfma_f32_16x16x32_bf16 v[120:123], v[132:135], v[172:175], 0
	v_mfma_f32_16x16x32_bf16 v[116:119], v[140:143], v[172:175], 0
	v_mfma_f32_16x16x32_bf16 v[88:91], v[132:135], v[180:183], 0
	v_mfma_f32_16x16x32_bf16 v[84:87], v[140:143], v[180:183], 0
	v_mfma_f32_16x16x32_bf16 v[72:75], v[132:135], v[188:191], 0
	v_mfma_f32_16x16x32_bf16 v[68:71], v[140:143], v[188:191], 0
	v_mfma_f32_16x16x32_bf16 v[152:155], v[136:139], v[168:171], v[152:155]
	v_mfma_f32_16x16x32_bf16 v[148:151], v[144:147], v[168:171], v[148:151]
	v_mfma_f32_16x16x32_bf16 v[120:123], v[136:139], v[176:179], v[120:123]
	v_mfma_f32_16x16x32_bf16 v[116:119], v[144:147], v[176:179], v[116:119]
	v_mfma_f32_16x16x32_bf16 v[88:91], v[136:139], v[184:187], v[88:91]
	v_mfma_f32_16x16x32_bf16 v[84:87], v[144:147], v[184:187], v[84:87]
	v_mfma_f32_16x16x32_bf16 v[72:75], v[136:139], v[192:195], v[72:75]
	v_mfma_f32_16x16x32_bf16 v[68:71], v[144:147], v[192:195], v[68:71]
	s_setprio 0
	s_barrier
	s_add_i32 s23, s34, s69
	v_lshl_add_u64 v[208:209], s[28:29], 0, v[200:201]
	s_mov_b32 m0, s23
	ds_read_b128 v[164:167], v240 offset:16384
	ds_read_b128 v[168:171], v240 offset:17408
	ds_read_b128 v[172:175], v240 offset:18432
	ds_read_b128 v[176:179], v240 offset:19456
	ds_read_b128 v[180:183], v240 offset:20480
	ds_read_b128 v[184:187], v240 offset:21504
	ds_read_b128 v[188:191], v240 offset:22528
	ds_read_b128 v[192:195], v240 offset:23552
	global_load_lds_dwordx4 v[208:209], off
	s_add_i32 m0, s23, 0x2000
	v_lshl_add_u64 v[210:211], s[28:29], 0, v[196:197]
	s_add_u32 s28, s28, s6
	s_addc_u32 s29, s29, s7
	s_add_i32 s21, s21, s69
	global_load_lds_dwordx4 v[210:211], off
	v_lshl_add_u64 v[218:219], s[28:29], 0, v[200:201]
	s_mov_b32 m0, s21
	v_lshl_add_u64 v[220:221], s[28:29], 0, v[196:197]
	global_load_lds_dwordx4 v[218:219], off
	s_add_i32 m0, s21, 0x2000
	v_lshl_add_u64 v[222:223], s[30:31], 0, v[202:203]
	global_load_lds_dwordx4 v[220:221], off
	s_mov_b32 m0, s72
	v_lshl_add_u64 v[224:225], s[30:31], 0, v[198:199]
	global_load_lds_dwordx4 v[222:223], off
	s_mov_b32 m0, s73
	s_nop 0
	global_load_lds_dwordx4 v[224:225], off
	s_waitcnt vmcnt(8)
	s_waitcnt lgkmcnt(0)
	s_barrier
	s_setprio 1
	s_waitcnt lgkmcnt(0)
	v_mfma_f32_16x16x32_bf16 v[64:67], v[100:103], v[164:167], 0
	v_mfma_f32_16x16x32_bf16 v[60:63], v[108:111], v[164:167], 0
	v_mfma_f32_16x16x32_bf16 v[48:51], v[100:103], v[172:175], 0
	v_mfma_f32_16x16x32_bf16 v[44:47], v[108:111], v[172:175], 0
	v_mfma_f32_16x16x32_bf16 v[32:35], v[100:103], v[180:183], 0
	v_mfma_f32_16x16x32_bf16 v[28:31], v[108:111], v[180:183], 0
	v_mfma_f32_16x16x32_bf16 v[16:19], v[100:103], v[188:191], 0
	v_mfma_f32_16x16x32_bf16 v[12:15], v[108:111], v[188:191], 0
	v_mfma_f32_16x16x32_bf16 v[64:67], v[104:107], v[168:171], v[64:67]
	v_mfma_f32_16x16x32_bf16 v[60:63], v[112:115], v[168:171], v[60:63]
	v_mfma_f32_16x16x32_bf16 v[48:51], v[104:107], v[176:179], v[48:51]
	v_mfma_f32_16x16x32_bf16 v[44:47], v[112:115], v[176:179], v[44:47]
	v_mfma_f32_16x16x32_bf16 v[32:35], v[104:107], v[184:187], v[32:35]
	v_mfma_f32_16x16x32_bf16 v[28:31], v[112:115], v[184:187], v[28:31]
	v_mfma_f32_16x16x32_bf16 v[16:19], v[104:107], v[192:195], v[16:19]
	v_mfma_f32_16x16x32_bf16 v[12:15], v[112:115], v[192:195], v[12:15]
	s_setprio 0
	s_setprio 1
	v_mfma_f32_16x16x32_bf16 v[56:59], v[132:135], v[164:167], 0
	v_mfma_f32_16x16x32_bf16 v[52:55], v[140:143], v[164:167], 0
	v_mfma_f32_16x16x32_bf16 v[40:43], v[132:135], v[172:175], 0
	v_mfma_f32_16x16x32_bf16 v[36:39], v[140:143], v[172:175], 0
	v_mfma_f32_16x16x32_bf16 v[24:27], v[132:135], v[180:183], 0
	v_mfma_f32_16x16x32_bf16 v[20:23], v[140:143], v[180:183], 0
	v_mfma_f32_16x16x32_bf16 v[8:11], v[132:135], v[188:191], 0
	v_mfma_f32_16x16x32_bf16 v[4:7], v[140:143], v[188:191], 0
	v_mfma_f32_16x16x32_bf16 v[56:59], v[136:139], v[168:171], v[56:59]
	v_mfma_f32_16x16x32_bf16 v[52:55], v[144:147], v[168:171], v[52:55]
	v_mfma_f32_16x16x32_bf16 v[40:43], v[136:139], v[176:179], v[40:43]
	v_mfma_f32_16x16x32_bf16 v[36:39], v[144:147], v[176:179], v[36:39]
	v_mfma_f32_16x16x32_bf16 v[24:27], v[136:139], v[184:187], v[24:27]
	v_mfma_f32_16x16x32_bf16 v[20:23], v[144:147], v[184:187], v[20:23]
	v_mfma_f32_16x16x32_bf16 v[8:11], v[136:139], v[192:195], v[8:11]
	v_mfma_f32_16x16x32_bf16 v[4:7], v[144:147], v[192:195], v[4:7]
	s_setprio 0
	s_barrier
	s_add_i32 s21, 0, 0x18000
	v_add_u32_e32 v2, s21, v231
	s_add_i32 s23, 0, 0x1c000
	ds_read_b128 v[100:103], v2
	ds_read_b128 v[104:107], v2 offset:1024
	ds_read_b128 v[108:111], v2 offset:2048
	ds_read_b128 v[112:115], v2 offset:3072
	v_add_u32_e32 v2, s23, v231
	ds_read_b128 v[132:135], v2
	ds_read_b128 v[136:139], v2 offset:1024
	ds_read_b128 v[140:143], v2 offset:2048
	ds_read_b128 v[144:147], v2 offset:3072
	s_add_u32 s28, s30, s6
	s_addc_u32 s29, s31, s7
	s_mov_b32 m0, s74
	v_lshl_add_u64 v[226:227], s[28:29], 0, v[202:203]
	ds_read_b128 v[164:167], v240 offset:32768
	ds_read_b128 v[168:171], v240 offset:33792
	ds_read_b128 v[172:175], v240 offset:34816
	ds_read_b128 v[176:179], v240 offset:35840
	ds_read_b128 v[180:183], v240 offset:36864
	ds_read_b128 v[184:187], v240 offset:37888
	ds_read_b128 v[188:191], v240 offset:38912
	ds_read_b128 v[192:195], v240 offset:39936
	global_load_lds_dwordx4 v[226:227], off
	v_lshl_add_u64 v[226:227], s[28:29], 0, v[198:199]
	s_mov_b32 m0, s75
	s_nop 0
	global_load_lds_dwordx4 v[226:227], off
	s_waitcnt vmcnt(8)
	s_waitcnt lgkmcnt(0)
	s_barrier
	s_setprio 1
	s_waitcnt lgkmcnt(0)
	v_mfma_f32_16x16x32_bf16 v[160:163], v[100:103], v[164:167], v[160:163]
	v_mfma_f32_16x16x32_bf16 v[156:159], v[108:111], v[164:167], v[156:159]
	v_mfma_f32_16x16x32_bf16 v[128:131], v[100:103], v[172:175], v[128:131]
	v_mfma_f32_16x16x32_bf16 v[124:127], v[108:111], v[172:175], v[124:127]
	v_mfma_f32_16x16x32_bf16 v[96:99], v[100:103], v[180:183], v[96:99]
	v_mfma_f32_16x16x32_bf16 v[92:95], v[108:111], v[180:183], v[92:95]
	v_mfma_f32_16x16x32_bf16 v[80:83], v[100:103], v[188:191], v[80:83]
	v_mfma_f32_16x16x32_bf16 v[76:79], v[108:111], v[188:191], v[76:79]
	v_mfma_f32_16x16x32_bf16 v[160:163], v[104:107], v[168:171], v[160:163]
	v_mfma_f32_16x16x32_bf16 v[156:159], v[112:115], v[168:171], v[156:159]
	v_mfma_f32_16x16x32_bf16 v[128:131], v[104:107], v[176:179], v[128:131]
	v_mfma_f32_16x16x32_bf16 v[124:127], v[112:115], v[176:179], v[124:127]
	v_mfma_f32_16x16x32_bf16 v[96:99], v[104:107], v[184:187], v[96:99]
	v_mfma_f32_16x16x32_bf16 v[92:95], v[112:115], v[184:187], v[92:95]
	v_mfma_f32_16x16x32_bf16 v[80:83], v[104:107], v[192:195], v[80:83]
	v_mfma_f32_16x16x32_bf16 v[76:79], v[112:115], v[192:195], v[76:79]
	s_setprio 0
	s_setprio 1
	v_mfma_f32_16x16x32_bf16 v[152:155], v[132:135], v[164:167], v[152:155]
	v_mfma_f32_16x16x32_bf16 v[148:151], v[140:143], v[164:167], v[148:151]
	v_mfma_f32_16x16x32_bf16 v[120:123], v[132:135], v[172:175], v[120:123]
	v_mfma_f32_16x16x32_bf16 v[116:119], v[140:143], v[172:175], v[116:119]
	v_mfma_f32_16x16x32_bf16 v[88:91], v[132:135], v[180:183], v[88:91]
	v_mfma_f32_16x16x32_bf16 v[84:87], v[140:143], v[180:183], v[84:87]
	v_mfma_f32_16x16x32_bf16 v[72:75], v[132:135], v[188:191], v[72:75]
	v_mfma_f32_16x16x32_bf16 v[68:71], v[140:143], v[188:191], v[68:71]
	v_mfma_f32_16x16x32_bf16 v[152:155], v[136:139], v[168:171], v[152:155]
	v_mfma_f32_16x16x32_bf16 v[148:151], v[144:147], v[168:171], v[148:151]
	v_mfma_f32_16x16x32_bf16 v[120:123], v[136:139], v[176:179], v[120:123]
	v_mfma_f32_16x16x32_bf16 v[116:119], v[144:147], v[176:179], v[116:119]
	v_mfma_f32_16x16x32_bf16 v[88:91], v[136:139], v[184:187], v[88:91]
	v_mfma_f32_16x16x32_bf16 v[84:87], v[144:147], v[184:187], v[84:87]
	v_mfma_f32_16x16x32_bf16 v[72:75], v[136:139], v[192:195], v[72:75]
	v_mfma_f32_16x16x32_bf16 v[68:71], v[144:147], v[192:195], v[68:71]
	s_setprio 0
	s_barrier
	s_add_i32 s21, s21, s69
	v_lshl_add_u64 v[208:209], v[208:209], 0, s[24:25]
	s_mov_b32 m0, s21
	ds_read_b128 v[164:167], v240 offset:49152
	ds_read_b128 v[168:171], v240 offset:50176
	ds_read_b128 v[172:175], v240 offset:51200
	ds_read_b128 v[176:179], v240 offset:52224
	ds_read_b128 v[180:183], v240 offset:53248
	ds_read_b128 v[184:187], v240 offset:54272
	ds_read_b128 v[188:191], v240 offset:55296
	ds_read_b128 v[192:195], v240 offset:56320
	global_load_lds_dwordx4 v[208:209], off
	v_lshl_add_u64 v[208:209], v[210:211], 0, s[24:25]
	s_add_i32 m0, s21, 0x2000
	s_add_i32 s21, s23, s69
	global_load_lds_dwordx4 v[208:209], off
	v_lshl_add_u64 v[208:209], v[218:219], 0, s[24:25]
	s_mov_b32 m0, s21
	s_nop 0
	global_load_lds_dwordx4 v[208:209], off
	v_lshl_add_u64 v[208:209], v[220:221], 0, s[24:25]
	s_add_i32 m0, s21, 0x2000
	s_nop 0
	global_load_lds_dwordx4 v[208:209], off
	v_lshl_add_u64 v[208:209], v[222:223], 0, s[24:25]
	s_mov_b32 m0, s79
	s_nop 0
	global_load_lds_dwordx4 v[208:209], off
	v_lshl_add_u64 v[208:209], v[224:225], 0, s[24:25]
	s_mov_b32 m0, s80
	s_nop 0
	global_load_lds_dwordx4 v[208:209], off
	s_waitcnt vmcnt(8)
	s_waitcnt lgkmcnt(0)
	s_barrier
	s_setprio 1
	s_waitcnt lgkmcnt(0)
	v_mfma_f32_16x16x32_bf16 v[64:67], v[100:103], v[164:167], v[64:67]
	v_mfma_f32_16x16x32_bf16 v[60:63], v[108:111], v[164:167], v[60:63]
	v_mfma_f32_16x16x32_bf16 v[48:51], v[100:103], v[172:175], v[48:51]
	v_mfma_f32_16x16x32_bf16 v[44:47], v[108:111], v[172:175], v[44:47]
	v_mfma_f32_16x16x32_bf16 v[32:35], v[100:103], v[180:183], v[32:35]
	v_mfma_f32_16x16x32_bf16 v[28:31], v[108:111], v[180:183], v[28:31]
	v_mfma_f32_16x16x32_bf16 v[16:19], v[100:103], v[188:191], v[16:19]
	v_mfma_f32_16x16x32_bf16 v[12:15], v[108:111], v[188:191], v[12:15]
	v_mfma_f32_16x16x32_bf16 v[64:67], v[104:107], v[168:171], v[64:67]
	v_mfma_f32_16x16x32_bf16 v[60:63], v[112:115], v[168:171], v[60:63]
	v_mfma_f32_16x16x32_bf16 v[48:51], v[104:107], v[176:179], v[48:51]
	v_mfma_f32_16x16x32_bf16 v[44:47], v[112:115], v[176:179], v[44:47]
	v_mfma_f32_16x16x32_bf16 v[32:35], v[104:107], v[184:187], v[32:35]
	v_mfma_f32_16x16x32_bf16 v[28:31], v[112:115], v[184:187], v[28:31]
	v_mfma_f32_16x16x32_bf16 v[16:19], v[104:107], v[192:195], v[16:19]
	v_mfma_f32_16x16x32_bf16 v[12:15], v[112:115], v[192:195], v[12:15]
	s_setprio 0
	s_setprio 1
	v_mfma_f32_16x16x32_bf16 v[56:59], v[132:135], v[164:167], v[56:59]
	v_mfma_f32_16x16x32_bf16 v[52:55], v[140:143], v[164:167], v[52:55]
	v_mfma_f32_16x16x32_bf16 v[40:43], v[132:135], v[172:175], v[40:43]
	v_mfma_f32_16x16x32_bf16 v[36:39], v[140:143], v[172:175], v[36:39]
	v_mfma_f32_16x16x32_bf16 v[24:27], v[132:135], v[180:183], v[24:27]
	v_mfma_f32_16x16x32_bf16 v[20:23], v[140:143], v[180:183], v[20:23]
	v_mfma_f32_16x16x32_bf16 v[8:11], v[132:135], v[188:191], v[8:11]
	v_mfma_f32_16x16x32_bf16 v[4:7], v[140:143], v[188:191], v[4:7]
	v_mfma_f32_16x16x32_bf16 v[56:59], v[136:139], v[168:171], v[56:59]
	v_mfma_f32_16x16x32_bf16 v[52:55], v[144:147], v[168:171], v[52:55]
	v_mfma_f32_16x16x32_bf16 v[40:43], v[136:139], v[176:179], v[40:43]
	v_mfma_f32_16x16x32_bf16 v[36:39], v[144:147], v[176:179], v[36:39]
	v_mfma_f32_16x16x32_bf16 v[24:27], v[136:139], v[184:187], v[24:27]
	v_mfma_f32_16x16x32_bf16 v[20:23], v[144:147], v[184:187], v[20:23]
	v_mfma_f32_16x16x32_bf16 v[8:11], v[136:139], v[192:195], v[8:11]
	v_mfma_f32_16x16x32_bf16 v[4:7], v[144:147], v[192:195], v[4:7]
	s_setprio 0
	s_barrier
	s_add_u32 s26, s26, 0x100
	s_addc_u32 s27, s27, 0
	s_add_u32 s19, s19, 0x100
	s_addc_u32 s20, s20, 0
	s_cmp_ge_i32 s22, s78
	s_mov_b32 s21, s22
	s_cbranch_scc1 .LBB0_812

.LBB0_1302:
	s_andn2_b64 vcc, exec, s[42:43]
	s_cbranch_vccnz .LBB0_1305
	s_add_u32 s2, s30, 0x80
	s_addc_u32 s3, s31, 0
	s_add_u32 s19, s26, 0x100
	s_addc_u32 s20, s27, 0
	s_mov_b32 s21, 0
	s_add_i32 s22, s21, 2
	s_add_u32 s23, s2, 0x80
	s_addc_u32 s26, s3, 0
	s_add_i32 s30, 0, 0x10000
	s_cmp_eq_u32 s64, s21
	s_cselect_b32 s27, s47, s26
	s_cselect_b32 s26, s46, s23
	s_cselect_b32 s29, s49, s20
	s_cselect_b32 s28, s48, s19
	s_add_i32 s21, 0, 0x14000
	v_add_u32_e32 v144, s30, v220
	v_add_u32_e32 v160, s21, v220
	ds_read_b128 v[132:135], v144
	ds_read_b128 v[136:139], v144 offset:1024
	ds_read_b128 v[140:143], v144 offset:2048
	ds_read_b128 v[144:147], v144 offset:3072
	ds_read_b128 v[148:151], v160
	ds_read_b128 v[152:155], v160 offset:1024
	ds_read_b128 v[156:159], v160 offset:2048
	ds_read_b128 v[160:163], v160 offset:3072
	v_lshl_add_u64 v[210:211], s[2:3], 0, v[198:199]
	s_add_i32 m0, s56, 0xc000
	ds_read_b128 v[164:167], v221
	ds_read_b128 v[168:171], v221 offset:1024
	ds_read_b128 v[172:175], v221 offset:2048
	ds_read_b128 v[176:179], v221 offset:3072
	ds_read_b128 v[180:183], v221 offset:4096
	ds_read_b128 v[184:187], v221 offset:5120
	ds_read_b128 v[202:205], v221 offset:6144
	ds_read_b128 v[206:209], v221 offset:7168
	global_load_lds_dwordx4 v[210:211], off
	v_lshl_add_u64 v[210:211], s[2:3], 0, v[200:201]
	s_add_i32 m0, s56, 0xe000
	s_nop 0
	global_load_lds_dwordx4 v[210:211], off
	s_waitcnt vmcnt(8)
	s_waitcnt lgkmcnt(0)
	s_barrier
	s_setprio 1
	s_waitcnt lgkmcnt(0)
	v_mfma_f32_16x16x32_bf16 v[124:127], v[132:135], v[164:167], 0
	v_mfma_f32_16x16x32_bf16 v[128:131], v[140:143], v[164:167], 0
	v_mfma_f32_16x16x32_bf16 v[112:115], v[132:135], v[172:175], 0
	v_mfma_f32_16x16x32_bf16 v[108:111], v[140:143], v[172:175], 0
	v_mfma_f32_16x16x32_bf16 v[96:99], v[132:135], v[180:183], 0
	v_mfma_f32_16x16x32_bf16 v[92:95], v[140:143], v[180:183], 0
	v_mfma_f32_16x16x32_bf16 v[80:83], v[132:135], v[202:205], 0
	v_mfma_f32_16x16x32_bf16 v[76:79], v[140:143], v[202:205], 0
	v_mfma_f32_16x16x32_bf16 v[124:127], v[136:139], v[168:171], v[124:127]
	v_mfma_f32_16x16x32_bf16 v[128:131], v[144:147], v[168:171], v[128:131]
	v_mfma_f32_16x16x32_bf16 v[112:115], v[136:139], v[176:179], v[112:115]
	v_mfma_f32_16x16x32_bf16 v[108:111], v[144:147], v[176:179], v[108:111]
	v_mfma_f32_16x16x32_bf16 v[96:99], v[136:139], v[184:187], v[96:99]
	v_mfma_f32_16x16x32_bf16 v[92:95], v[144:147], v[184:187], v[92:95]
	v_mfma_f32_16x16x32_bf16 v[80:83], v[136:139], v[206:209], v[80:83]
	v_mfma_f32_16x16x32_bf16 v[76:79], v[144:147], v[206:209], v[76:79]
	s_setprio 0
	s_setprio 1
	v_mfma_f32_16x16x32_bf16 v[120:123], v[148:151], v[164:167], 0
	v_mfma_f32_16x16x32_bf16 v[116:119], v[156:159], v[164:167], 0
	v_mfma_f32_16x16x32_bf16 v[104:107], v[148:151], v[172:175], 0
	v_mfma_f32_16x16x32_bf16 v[100:103], v[156:159], v[172:175], 0
	v_mfma_f32_16x16x32_bf16 v[88:91], v[148:151], v[180:183], 0
	v_mfma_f32_16x16x32_bf16 v[84:87], v[156:159], v[180:183], 0
	v_mfma_f32_16x16x32_bf16 v[72:75], v[148:151], v[202:205], 0
	v_mfma_f32_16x16x32_bf16 v[68:71], v[156:159], v[202:205], 0
	v_mfma_f32_16x16x32_bf16 v[120:123], v[152:155], v[168:171], v[120:123]
	v_mfma_f32_16x16x32_bf16 v[116:119], v[160:163], v[168:171], v[116:119]
	v_mfma_f32_16x16x32_bf16 v[104:107], v[152:155], v[176:179], v[104:107]
	v_mfma_f32_16x16x32_bf16 v[100:103], v[160:163], v[176:179], v[100:103]
	v_mfma_f32_16x16x32_bf16 v[88:91], v[152:155], v[184:187], v[88:91]
	v_mfma_f32_16x16x32_bf16 v[84:87], v[160:163], v[184:187], v[84:87]
	v_mfma_f32_16x16x32_bf16 v[72:75], v[152:155], v[206:209], v[72:75]
	v_mfma_f32_16x16x32_bf16 v[68:71], v[160:163], v[206:209], v[68:71]
	s_setprio 0
	s_barrier
	s_add_i32 s23, s30, s55
	v_lshl_add_u64 v[210:211], s[28:29], 0, v[2:3]
	s_mov_b32 m0, s23
	ds_read_b128 v[164:167], v221 offset:16384
	ds_read_b128 v[168:171], v221 offset:17408
	ds_read_b128 v[172:175], v221 offset:18432
	ds_read_b128 v[176:179], v221 offset:19456
	ds_read_b128 v[180:183], v221 offset:20480
	ds_read_b128 v[184:187], v221 offset:21504
	ds_read_b128 v[202:205], v221 offset:22528
	ds_read_b128 v[206:209], v221 offset:23552
	global_load_lds_dwordx4 v[210:211], off
	s_add_i32 m0, s23, 0x2000
	v_lshl_add_u64 v[212:213], s[28:29], 0, v[188:189]
	s_add_u32 s28, s28, s8
	s_addc_u32 s29, s29, s9
	s_add_i32 s21, s21, s55
	global_load_lds_dwordx4 v[212:213], off
	v_lshl_add_u64 v[214:215], s[28:29], 0, v[2:3]
	s_mov_b32 m0, s21
	v_lshl_add_u64 v[222:223], s[28:29], 0, v[188:189]
	global_load_lds_dwordx4 v[214:215], off
	s_add_i32 m0, s21, 0x2000
	v_lshl_add_u64 v[224:225], s[26:27], 0, v[192:193]
	global_load_lds_dwordx4 v[222:223], off
	s_mov_b32 m0, s56
	v_lshl_add_u64 v[226:227], s[26:27], 0, v[190:191]
	global_load_lds_dwordx4 v[224:225], off
	s_mov_b32 m0, s57
	s_nop 0
	global_load_lds_dwordx4 v[226:227], off
	s_waitcnt vmcnt(8)
	s_waitcnt lgkmcnt(0)
	s_barrier
	s_setprio 1
	s_waitcnt lgkmcnt(0)
	v_mfma_f32_16x16x32_bf16 v[64:67], v[132:135], v[164:167], 0
	v_mfma_f32_16x16x32_bf16 v[60:63], v[140:143], v[164:167], 0
	v_mfma_f32_16x16x32_bf16 v[48:51], v[132:135], v[172:175], 0
	v_mfma_f32_16x16x32_bf16 v[44:47], v[140:143], v[172:175], 0
	v_mfma_f32_16x16x32_bf16 v[32:35], v[132:135], v[180:183], 0
	v_mfma_f32_16x16x32_bf16 v[28:31], v[140:143], v[180:183], 0
	v_mfma_f32_16x16x32_bf16 v[16:19], v[132:135], v[202:205], 0
	v_mfma_f32_16x16x32_bf16 v[12:15], v[140:143], v[202:205], 0
	v_mfma_f32_16x16x32_bf16 v[64:67], v[136:139], v[168:171], v[64:67]
	v_mfma_f32_16x16x32_bf16 v[60:63], v[144:147], v[168:171], v[60:63]
	v_mfma_f32_16x16x32_bf16 v[48:51], v[136:139], v[176:179], v[48:51]
	v_mfma_f32_16x16x32_bf16 v[44:47], v[144:147], v[176:179], v[44:47]
	v_mfma_f32_16x16x32_bf16 v[32:35], v[136:139], v[184:187], v[32:35]
	v_mfma_f32_16x16x32_bf16 v[28:31], v[144:147], v[184:187], v[28:31]
	v_mfma_f32_16x16x32_bf16 v[16:19], v[136:139], v[206:209], v[16:19]
	v_mfma_f32_16x16x32_bf16 v[12:15], v[144:147], v[206:209], v[12:15]
	s_setprio 0
	s_setprio 1
	v_mfma_f32_16x16x32_bf16 v[56:59], v[148:151], v[164:167], 0
	v_mfma_f32_16x16x32_bf16 v[52:55], v[156:159], v[164:167], 0
	v_mfma_f32_16x16x32_bf16 v[40:43], v[148:151], v[172:175], 0
	v_mfma_f32_16x16x32_bf16 v[36:39], v[156:159], v[172:175], 0
	v_mfma_f32_16x16x32_bf16 v[24:27], v[148:151], v[180:183], 0
	v_mfma_f32_16x16x32_bf16 v[20:23], v[156:159], v[180:183], 0
	v_mfma_f32_16x16x32_bf16 v[8:11], v[148:151], v[202:205], 0
	v_mfma_f32_16x16x32_bf16 v[4:7], v[156:159], v[202:205], 0
	v_mfma_f32_16x16x32_bf16 v[56:59], v[152:155], v[168:171], v[56:59]
	v_mfma_f32_16x16x32_bf16 v[52:55], v[160:163], v[168:171], v[52:55]
	v_mfma_f32_16x16x32_bf16 v[40:43], v[152:155], v[176:179], v[40:43]
	v_mfma_f32_16x16x32_bf16 v[36:39], v[160:163], v[176:179], v[36:39]
	v_mfma_f32_16x16x32_bf16 v[24:27], v[152:155], v[184:187], v[24:27]
	v_mfma_f32_16x16x32_bf16 v[20:23], v[160:163], v[184:187], v[20:23]
	v_mfma_f32_16x16x32_bf16 v[8:11], v[152:155], v[206:209], v[8:11]
	v_mfma_f32_16x16x32_bf16 v[4:7], v[160:163], v[206:209], v[4:7]
	s_setprio 0
	s_barrier
	s_add_i32 s21, 0, 0x18000
	s_add_i32 s23, 0, 0x1c000
	v_add_u32_e32 v144, s21, v220
	v_add_u32_e32 v160, s23, v220
	ds_read_b128 v[132:135], v144
	ds_read_b128 v[136:139], v144 offset:1024
	ds_read_b128 v[140:143], v144 offset:2048
	ds_read_b128 v[144:147], v144 offset:3072
	ds_read_b128 v[148:151], v160
	ds_read_b128 v[152:155], v160 offset:1024
	ds_read_b128 v[156:159], v160 offset:2048
	ds_read_b128 v[160:163], v160 offset:3072
	s_add_u32 s26, s26, s8
	s_addc_u32 s27, s27, s9
	s_mov_b32 m0, s58
	v_lshl_add_u64 v[228:229], s[26:27], 0, v[192:193]
	ds_read_b128 v[164:167], v221 offset:32768
	ds_read_b128 v[168:171], v221 offset:33792
	ds_read_b128 v[172:175], v221 offset:34816
	ds_read_b128 v[176:179], v221 offset:35840
	ds_read_b128 v[180:183], v221 offset:36864
	ds_read_b128 v[184:187], v221 offset:37888
	ds_read_b128 v[202:205], v221 offset:38912
	ds_read_b128 v[206:209], v221 offset:39936
	global_load_lds_dwordx4 v[228:229], off
	v_lshl_add_u64 v[228:229], s[26:27], 0, v[190:191]
	s_mov_b32 m0, s59
	s_nop 0
	global_load_lds_dwordx4 v[228:229], off
	s_waitcnt vmcnt(8)
	s_waitcnt lgkmcnt(0)
	s_barrier
	s_setprio 1
	s_waitcnt lgkmcnt(0)
	v_mfma_f32_16x16x32_bf16 v[124:127], v[132:135], v[164:167], v[124:127]
	v_mfma_f32_16x16x32_bf16 v[128:131], v[140:143], v[164:167], v[128:131]
	v_mfma_f32_16x16x32_bf16 v[112:115], v[132:135], v[172:175], v[112:115]
	v_mfma_f32_16x16x32_bf16 v[108:111], v[140:143], v[172:175], v[108:111]
	v_mfma_f32_16x16x32_bf16 v[96:99], v[132:135], v[180:183], v[96:99]
	v_mfma_f32_16x16x32_bf16 v[92:95], v[140:143], v[180:183], v[92:95]
	v_mfma_f32_16x16x32_bf16 v[80:83], v[132:135], v[202:205], v[80:83]
	v_mfma_f32_16x16x32_bf16 v[76:79], v[140:143], v[202:205], v[76:79]
	v_mfma_f32_16x16x32_bf16 v[124:127], v[136:139], v[168:171], v[124:127]
	v_mfma_f32_16x16x32_bf16 v[128:131], v[144:147], v[168:171], v[128:131]
	v_mfma_f32_16x16x32_bf16 v[112:115], v[136:139], v[176:179], v[112:115]
	v_mfma_f32_16x16x32_bf16 v[108:111], v[144:147], v[176:179], v[108:111]
	v_mfma_f32_16x16x32_bf16 v[96:99], v[136:139], v[184:187], v[96:99]
	v_mfma_f32_16x16x32_bf16 v[92:95], v[144:147], v[184:187], v[92:95]
	v_mfma_f32_16x16x32_bf16 v[80:83], v[136:139], v[206:209], v[80:83]
	v_mfma_f32_16x16x32_bf16 v[76:79], v[144:147], v[206:209], v[76:79]
	s_setprio 0
	s_setprio 1
	v_mfma_f32_16x16x32_bf16 v[120:123], v[148:151], v[164:167], v[120:123]
	v_mfma_f32_16x16x32_bf16 v[116:119], v[156:159], v[164:167], v[116:119]
	v_mfma_f32_16x16x32_bf16 v[104:107], v[148:151], v[172:175], v[104:107]
	v_mfma_f32_16x16x32_bf16 v[100:103], v[156:159], v[172:175], v[100:103]
	v_mfma_f32_16x16x32_bf16 v[88:91], v[148:151], v[180:183], v[88:91]
	v_mfma_f32_16x16x32_bf16 v[84:87], v[156:159], v[180:183], v[84:87]
	v_mfma_f32_16x16x32_bf16 v[72:75], v[148:151], v[202:205], v[72:75]
	v_mfma_f32_16x16x32_bf16 v[68:71], v[156:159], v[202:205], v[68:71]
	v_mfma_f32_16x16x32_bf16 v[120:123], v[152:155], v[168:171], v[120:123]
	v_mfma_f32_16x16x32_bf16 v[116:119], v[160:163], v[168:171], v[116:119]
	v_mfma_f32_16x16x32_bf16 v[104:107], v[152:155], v[176:179], v[104:107]
	v_mfma_f32_16x16x32_bf16 v[100:103], v[160:163], v[176:179], v[100:103]
	v_mfma_f32_16x16x32_bf16 v[88:91], v[152:155], v[184:187], v[88:91]
	v_mfma_f32_16x16x32_bf16 v[84:87], v[160:163], v[184:187], v[84:87]
	v_mfma_f32_16x16x32_bf16 v[72:75], v[152:155], v[206:209], v[72:75]
	v_mfma_f32_16x16x32_bf16 v[68:71], v[160:163], v[206:209], v[68:71]
	s_setprio 0
	s_barrier
	s_add_i32 s21, s21, s55
	v_lshl_add_u64 v[210:211], v[210:211], 0, s[24:25]
	s_mov_b32 m0, s21
	ds_read_b128 v[164:167], v221 offset:49152
	ds_read_b128 v[168:171], v221 offset:50176
	ds_read_b128 v[172:175], v221 offset:51200
	ds_read_b128 v[176:179], v221 offset:52224
	ds_read_b128 v[180:183], v221 offset:53248
	ds_read_b128 v[184:187], v221 offset:54272
	ds_read_b128 v[202:205], v221 offset:55296
	ds_read_b128 v[206:209], v221 offset:56320
	global_load_lds_dwordx4 v[210:211], off
	v_lshl_add_u64 v[210:211], v[212:213], 0, s[24:25]
	s_add_i32 m0, s21, 0x2000
	s_add_i32 s21, s23, s55
	global_load_lds_dwordx4 v[210:211], off
	v_lshl_add_u64 v[210:211], v[214:215], 0, s[24:25]
	s_mov_b32 m0, s21
	s_nop 0
	global_load_lds_dwordx4 v[210:211], off
	v_lshl_add_u64 v[210:211], v[222:223], 0, s[24:25]
	s_add_i32 m0, s21, 0x2000
	s_nop 0
	global_load_lds_dwordx4 v[210:211], off
	v_lshl_add_u64 v[210:211], v[224:225], 0, s[24:25]
	s_mov_b32 m0, s60
	s_nop 0
	global_load_lds_dwordx4 v[210:211], off
	v_lshl_add_u64 v[210:211], v[226:227], 0, s[24:25]
	s_mov_b32 m0, s61
	s_nop 0
	global_load_lds_dwordx4 v[210:211], off
	s_waitcnt vmcnt(8)
	s_waitcnt lgkmcnt(0)
	s_barrier
	s_setprio 1
	s_waitcnt lgkmcnt(0)
	v_mfma_f32_16x16x32_bf16 v[64:67], v[132:135], v[164:167], v[64:67]
	v_mfma_f32_16x16x32_bf16 v[60:63], v[140:143], v[164:167], v[60:63]
	v_mfma_f32_16x16x32_bf16 v[48:51], v[132:135], v[172:175], v[48:51]
	v_mfma_f32_16x16x32_bf16 v[44:47], v[140:143], v[172:175], v[44:47]
	v_mfma_f32_16x16x32_bf16 v[32:35], v[132:135], v[180:183], v[32:35]
	v_mfma_f32_16x16x32_bf16 v[28:31], v[140:143], v[180:183], v[28:31]
	v_mfma_f32_16x16x32_bf16 v[16:19], v[132:135], v[202:205], v[16:19]
	v_mfma_f32_16x16x32_bf16 v[12:15], v[140:143], v[202:205], v[12:15]
	v_mfma_f32_16x16x32_bf16 v[64:67], v[136:139], v[168:171], v[64:67]
	v_mfma_f32_16x16x32_bf16 v[60:63], v[144:147], v[168:171], v[60:63]
	v_mfma_f32_16x16x32_bf16 v[48:51], v[136:139], v[176:179], v[48:51]
	v_mfma_f32_16x16x32_bf16 v[44:47], v[144:147], v[176:179], v[44:47]
	v_mfma_f32_16x16x32_bf16 v[32:35], v[136:139], v[184:187], v[32:35]
	v_mfma_f32_16x16x32_bf16 v[28:31], v[144:147], v[184:187], v[28:31]
	v_mfma_f32_16x16x32_bf16 v[16:19], v[136:139], v[206:209], v[16:19]
	v_mfma_f32_16x16x32_bf16 v[12:15], v[144:147], v[206:209], v[12:15]
	s_setprio 0
	s_setprio 1
	v_mfma_f32_16x16x32_bf16 v[56:59], v[148:151], v[164:167], v[56:59]
	v_mfma_f32_16x16x32_bf16 v[52:55], v[156:159], v[164:167], v[52:55]
	v_mfma_f32_16x16x32_bf16 v[40:43], v[148:151], v[172:175], v[40:43]
	v_mfma_f32_16x16x32_bf16 v[36:39], v[156:159], v[172:175], v[36:39]
	v_mfma_f32_16x16x32_bf16 v[24:27], v[148:151], v[180:183], v[24:27]
	v_mfma_f32_16x16x32_bf16 v[20:23], v[156:159], v[180:183], v[20:23]
	v_mfma_f32_16x16x32_bf16 v[8:11], v[148:151], v[202:205], v[8:11]
	v_mfma_f32_16x16x32_bf16 v[4:7], v[156:159], v[202:205], v[4:7]
	v_mfma_f32_16x16x32_bf16 v[56:59], v[152:155], v[168:171], v[56:59]
	v_mfma_f32_16x16x32_bf16 v[52:55], v[160:163], v[168:171], v[52:55]
	v_mfma_f32_16x16x32_bf16 v[40:43], v[152:155], v[176:179], v[40:43]
	v_mfma_f32_16x16x32_bf16 v[36:39], v[160:163], v[176:179], v[36:39]
	v_mfma_f32_16x16x32_bf16 v[24:27], v[152:155], v[184:187], v[24:27]
	v_mfma_f32_16x16x32_bf16 v[20:23], v[160:163], v[184:187], v[20:23]
	v_mfma_f32_16x16x32_bf16 v[8:11], v[152:155], v[206:209], v[8:11]
	v_mfma_f32_16x16x32_bf16 v[4:7], v[160:163], v[206:209], v[4:7]
	s_setprio 0
	s_barrier
	s_add_u32 s2, s2, 0x100
	s_addc_u32 s3, s3, 0
	s_add_u32 s19, s19, 0x100
	s_addc_u32 s20, s20, 0
	s_cmp_ge_i32 s22, s62
	s_mov_b32 s21, s22
	s_cbranch_scc1 .LBB0_1305

.LBB0_1327:
	s_andn2_b64 vcc, exec, s[16:17]
	s_waitcnt lgkmcnt(0)
	s_cbranch_vccnz .LBB0_1330
	s_add_u32 s2, s30, 0x80
	s_addc_u32 s3, s31, 0
	s_add_u32 s19, s26, 0x100
	s_addc_u32 s20, s27, 0
	s_mov_b32 s21, 0
	s_add_i32 s22, s21, 2
	s_add_u32 s23, s2, 0x80
	s_addc_u32 s26, s3, 0
	s_add_i32 s30, 0, 0x10000
	s_cmp_eq_u32 s63, s21
	s_cselect_b32 s27, s45, s26
	s_cselect_b32 s26, s44, s23
	s_cselect_b32 s29, s47, s20
	s_cselect_b32 s28, s46, s19
	s_add_i32 s21, 0, 0x14000
	v_add_u32_e32 v154, s30, v166
	v_add_u32_e32 v162, s21, v166
	ds_read_b128 v[132:135], v154
	ds_read_b128 v[136:139], v154 offset:1024
	ds_read_b128 v[140:143], v154 offset:2048
	ds_read_b128 v[154:157], v154 offset:3072
	ds_read_b128 v[158:161], v162
	ds_read_b128 v[170:173], v162 offset:1024
	ds_read_b128 v[174:177], v162 offset:2048
	ds_read_b128 v[178:181], v162 offset:3072
	v_lshl_add_u64 v[162:163], s[2:3], 0, v[150:151]
	s_add_i32 m0, s53, 0xc000
	ds_read_b128 v[182:185], v168
	ds_read_b128 v[186:189], v168 offset:1024
	ds_read_b128 v[190:193], v168 offset:2048
	ds_read_b128 v[194:197], v168 offset:3072
	ds_read_b128 v[198:201], v168 offset:4096
	ds_read_b128 v[202:205], v168 offset:5120
	ds_read_b128 v[206:209], v168 offset:6144
	ds_read_b128 v[218:221], v168 offset:7168
	global_load_lds_dwordx4 v[162:163], off
	v_lshl_add_u64 v[162:163], s[2:3], 0, v[152:153]
	s_add_i32 m0, s53, 0xe000
	s_nop 0
	global_load_lds_dwordx4 v[162:163], off
	s_waitcnt vmcnt(8)
	s_waitcnt lgkmcnt(0)
	s_barrier
	s_setprio 1
	s_waitcnt lgkmcnt(0)
	v_mfma_f32_16x16x32_bf16 v[128:131], v[132:135], v[182:185], 0
	v_mfma_f32_16x16x32_bf16 v[124:127], v[140:143], v[182:185], 0
	v_mfma_f32_16x16x32_bf16 v[112:115], v[132:135], v[190:193], 0
	v_mfma_f32_16x16x32_bf16 v[108:111], v[140:143], v[190:193], 0
	v_mfma_f32_16x16x32_bf16 v[96:99], v[132:135], v[198:201], 0
	v_mfma_f32_16x16x32_bf16 v[92:95], v[140:143], v[198:201], 0
	v_mfma_f32_16x16x32_bf16 v[80:83], v[132:135], v[206:209], 0
	v_mfma_f32_16x16x32_bf16 v[76:79], v[140:143], v[206:209], 0
	v_mfma_f32_16x16x32_bf16 v[128:131], v[136:139], v[186:189], v[128:131]
	v_mfma_f32_16x16x32_bf16 v[124:127], v[154:157], v[186:189], v[124:127]
	v_mfma_f32_16x16x32_bf16 v[112:115], v[136:139], v[194:197], v[112:115]
	v_mfma_f32_16x16x32_bf16 v[108:111], v[154:157], v[194:197], v[108:111]
	v_mfma_f32_16x16x32_bf16 v[96:99], v[136:139], v[202:205], v[96:99]
	v_mfma_f32_16x16x32_bf16 v[92:95], v[154:157], v[202:205], v[92:95]
	v_mfma_f32_16x16x32_bf16 v[80:83], v[136:139], v[218:221], v[80:83]
	v_mfma_f32_16x16x32_bf16 v[76:79], v[154:157], v[218:221], v[76:79]
	s_setprio 0
	s_setprio 1
	v_mfma_f32_16x16x32_bf16 v[120:123], v[158:161], v[182:185], 0
	v_mfma_f32_16x16x32_bf16 v[116:119], v[174:177], v[182:185], 0
	v_mfma_f32_16x16x32_bf16 v[104:107], v[158:161], v[190:193], 0
	v_mfma_f32_16x16x32_bf16 v[100:103], v[174:177], v[190:193], 0
	v_mfma_f32_16x16x32_bf16 v[88:91], v[158:161], v[198:201], 0
	v_mfma_f32_16x16x32_bf16 v[84:87], v[174:177], v[198:201], 0
	v_mfma_f32_16x16x32_bf16 v[72:75], v[158:161], v[206:209], 0
	v_mfma_f32_16x16x32_bf16 v[68:71], v[174:177], v[206:209], 0
	v_mfma_f32_16x16x32_bf16 v[120:123], v[170:173], v[186:189], v[120:123]
	v_mfma_f32_16x16x32_bf16 v[116:119], v[178:181], v[186:189], v[116:119]
	v_mfma_f32_16x16x32_bf16 v[104:107], v[170:173], v[194:197], v[104:107]
	v_mfma_f32_16x16x32_bf16 v[100:103], v[178:181], v[194:197], v[100:103]
	v_mfma_f32_16x16x32_bf16 v[88:91], v[170:173], v[202:205], v[88:91]
	v_mfma_f32_16x16x32_bf16 v[84:87], v[178:181], v[202:205], v[84:87]
	v_mfma_f32_16x16x32_bf16 v[72:75], v[170:173], v[218:221], v[72:75]
	v_mfma_f32_16x16x32_bf16 v[68:71], v[178:181], v[218:221], v[68:71]
	s_setprio 0
	s_barrier
	s_add_i32 s23, s30, s52
	v_lshl_add_u64 v[162:163], s[28:29], 0, v[2:3]
	s_mov_b32 m0, s23
	ds_read_b128 v[182:185], v168 offset:16384
	ds_read_b128 v[186:189], v168 offset:17408
	ds_read_b128 v[190:193], v168 offset:18432
	ds_read_b128 v[194:197], v168 offset:19456
	ds_read_b128 v[198:201], v168 offset:20480
	ds_read_b128 v[202:205], v168 offset:21504
	ds_read_b128 v[206:209], v168 offset:22528
	ds_read_b128 v[218:221], v168 offset:23552
	global_load_lds_dwordx4 v[162:163], off
	s_add_i32 m0, s23, 0x2000
	v_lshl_add_u64 v[210:211], s[28:29], 0, v[144:145]
	s_add_u32 s28, s28, s8
	s_addc_u32 s29, s29, s9
	s_add_i32 s21, s21, s52
	global_load_lds_dwordx4 v[210:211], off
	v_lshl_add_u64 v[212:213], s[28:29], 0, v[2:3]
	s_mov_b32 m0, s21
	v_lshl_add_u64 v[214:215], s[28:29], 0, v[144:145]
	global_load_lds_dwordx4 v[212:213], off
	s_add_i32 m0, s21, 0x2000
	v_lshl_add_u64 v[222:223], s[26:27], 0, v[148:149]
	global_load_lds_dwordx4 v[214:215], off
	s_mov_b32 m0, s53
	v_lshl_add_u64 v[224:225], s[26:27], 0, v[146:147]
	global_load_lds_dwordx4 v[222:223], off
	s_mov_b32 m0, s54
	s_nop 0
	global_load_lds_dwordx4 v[224:225], off
	s_waitcnt vmcnt(8)
	s_waitcnt lgkmcnt(0)
	s_barrier
	s_setprio 1
	s_waitcnt lgkmcnt(0)
	v_mfma_f32_16x16x32_bf16 v[64:67], v[132:135], v[182:185], 0
	v_mfma_f32_16x16x32_bf16 v[60:63], v[140:143], v[182:185], 0
	v_mfma_f32_16x16x32_bf16 v[48:51], v[132:135], v[190:193], 0
	v_mfma_f32_16x16x32_bf16 v[44:47], v[140:143], v[190:193], 0
	v_mfma_f32_16x16x32_bf16 v[32:35], v[132:135], v[198:201], 0
	v_mfma_f32_16x16x32_bf16 v[28:31], v[140:143], v[198:201], 0
	v_mfma_f32_16x16x32_bf16 v[16:19], v[132:135], v[206:209], 0
	v_mfma_f32_16x16x32_bf16 v[12:15], v[140:143], v[206:209], 0
	v_mfma_f32_16x16x32_bf16 v[64:67], v[136:139], v[186:189], v[64:67]
	v_mfma_f32_16x16x32_bf16 v[60:63], v[154:157], v[186:189], v[60:63]
	v_mfma_f32_16x16x32_bf16 v[48:51], v[136:139], v[194:197], v[48:51]
	v_mfma_f32_16x16x32_bf16 v[44:47], v[154:157], v[194:197], v[44:47]
	v_mfma_f32_16x16x32_bf16 v[32:35], v[136:139], v[202:205], v[32:35]
	v_mfma_f32_16x16x32_bf16 v[28:31], v[154:157], v[202:205], v[28:31]
	v_mfma_f32_16x16x32_bf16 v[16:19], v[136:139], v[218:221], v[16:19]
	v_mfma_f32_16x16x32_bf16 v[12:15], v[154:157], v[218:221], v[12:15]
	s_setprio 0
	s_setprio 1
	v_mfma_f32_16x16x32_bf16 v[56:59], v[158:161], v[182:185], 0
	v_mfma_f32_16x16x32_bf16 v[52:55], v[174:177], v[182:185], 0
	v_mfma_f32_16x16x32_bf16 v[40:43], v[158:161], v[190:193], 0
	v_mfma_f32_16x16x32_bf16 v[36:39], v[174:177], v[190:193], 0
	v_mfma_f32_16x16x32_bf16 v[24:27], v[158:161], v[198:201], 0
	v_mfma_f32_16x16x32_bf16 v[20:23], v[174:177], v[198:201], 0
	v_mfma_f32_16x16x32_bf16 v[8:11], v[158:161], v[206:209], 0
	v_mfma_f32_16x16x32_bf16 v[4:7], v[174:177], v[206:209], 0
	v_mfma_f32_16x16x32_bf16 v[56:59], v[170:173], v[186:189], v[56:59]
	v_mfma_f32_16x16x32_bf16 v[52:55], v[178:181], v[186:189], v[52:55]
	v_mfma_f32_16x16x32_bf16 v[40:43], v[170:173], v[194:197], v[40:43]
	v_mfma_f32_16x16x32_bf16 v[36:39], v[178:181], v[194:197], v[36:39]
	v_mfma_f32_16x16x32_bf16 v[24:27], v[170:173], v[202:205], v[24:27]
	v_mfma_f32_16x16x32_bf16 v[20:23], v[178:181], v[202:205], v[20:23]
	v_mfma_f32_16x16x32_bf16 v[8:11], v[170:173], v[218:221], v[8:11]
	v_mfma_f32_16x16x32_bf16 v[4:7], v[178:181], v[218:221], v[4:7]
	s_setprio 0
	s_barrier
	s_add_i32 s21, 0, 0x18000
	s_add_i32 s23, 0, 0x1c000
	v_add_u32_e32 v154, s21, v166
	v_add_u32_e32 v164, s23, v166
	ds_read_b128 v[132:135], v154
	ds_read_b128 v[136:139], v154 offset:1024
	ds_read_b128 v[140:143], v154 offset:2048
	ds_read_b128 v[154:157], v154 offset:3072
	ds_read_b128 v[158:161], v164
	ds_read_b128 v[170:173], v164 offset:1024
	ds_read_b128 v[174:177], v164 offset:2048
	ds_read_b128 v[178:181], v164 offset:3072
	s_add_u32 s26, s26, s8
	s_addc_u32 s27, s27, s9
	s_mov_b32 m0, s55
	v_lshl_add_u64 v[226:227], s[26:27], 0, v[148:149]
	ds_read_b128 v[182:185], v168 offset:32768
	ds_read_b128 v[186:189], v168 offset:33792
	ds_read_b128 v[190:193], v168 offset:34816
	ds_read_b128 v[194:197], v168 offset:35840
	ds_read_b128 v[198:201], v168 offset:36864
	ds_read_b128 v[202:205], v168 offset:37888
	ds_read_b128 v[206:209], v168 offset:38912
	ds_read_b128 v[218:221], v168 offset:39936
	global_load_lds_dwordx4 v[226:227], off
	v_lshl_add_u64 v[226:227], s[26:27], 0, v[146:147]
	s_mov_b32 m0, s56
	s_nop 0
	global_load_lds_dwordx4 v[226:227], off
	s_waitcnt vmcnt(8)
	s_waitcnt lgkmcnt(0)
	s_barrier
	s_setprio 1
	s_waitcnt lgkmcnt(0)
	v_mfma_f32_16x16x32_bf16 v[128:131], v[132:135], v[182:185], v[128:131]
	v_mfma_f32_16x16x32_bf16 v[124:127], v[140:143], v[182:185], v[124:127]
	v_mfma_f32_16x16x32_bf16 v[112:115], v[132:135], v[190:193], v[112:115]
	v_mfma_f32_16x16x32_bf16 v[108:111], v[140:143], v[190:193], v[108:111]
	v_mfma_f32_16x16x32_bf16 v[96:99], v[132:135], v[198:201], v[96:99]
	v_mfma_f32_16x16x32_bf16 v[92:95], v[140:143], v[198:201], v[92:95]
	v_mfma_f32_16x16x32_bf16 v[80:83], v[132:135], v[206:209], v[80:83]
	v_mfma_f32_16x16x32_bf16 v[76:79], v[140:143], v[206:209], v[76:79]
	v_mfma_f32_16x16x32_bf16 v[128:131], v[136:139], v[186:189], v[128:131]
	v_mfma_f32_16x16x32_bf16 v[124:127], v[154:157], v[186:189], v[124:127]
	v_mfma_f32_16x16x32_bf16 v[112:115], v[136:139], v[194:197], v[112:115]
	v_mfma_f32_16x16x32_bf16 v[108:111], v[154:157], v[194:197], v[108:111]
	v_mfma_f32_16x16x32_bf16 v[96:99], v[136:139], v[202:205], v[96:99]
	v_mfma_f32_16x16x32_bf16 v[92:95], v[154:157], v[202:205], v[92:95]
	v_mfma_f32_16x16x32_bf16 v[80:83], v[136:139], v[218:221], v[80:83]
	v_mfma_f32_16x16x32_bf16 v[76:79], v[154:157], v[218:221], v[76:79]
	s_setprio 0
	s_setprio 1
	v_mfma_f32_16x16x32_bf16 v[120:123], v[158:161], v[182:185], v[120:123]
	v_mfma_f32_16x16x32_bf16 v[116:119], v[174:177], v[182:185], v[116:119]
	v_mfma_f32_16x16x32_bf16 v[104:107], v[158:161], v[190:193], v[104:107]
	v_mfma_f32_16x16x32_bf16 v[100:103], v[174:177], v[190:193], v[100:103]
	v_mfma_f32_16x16x32_bf16 v[88:91], v[158:161], v[198:201], v[88:91]
	v_mfma_f32_16x16x32_bf16 v[84:87], v[174:177], v[198:201], v[84:87]
	v_mfma_f32_16x16x32_bf16 v[72:75], v[158:161], v[206:209], v[72:75]
	v_mfma_f32_16x16x32_bf16 v[68:71], v[174:177], v[206:209], v[68:71]
	v_mfma_f32_16x16x32_bf16 v[120:123], v[170:173], v[186:189], v[120:123]
	v_mfma_f32_16x16x32_bf16 v[116:119], v[178:181], v[186:189], v[116:119]
	v_mfma_f32_16x16x32_bf16 v[104:107], v[170:173], v[194:197], v[104:107]
	v_mfma_f32_16x16x32_bf16 v[100:103], v[178:181], v[194:197], v[100:103]
	v_mfma_f32_16x16x32_bf16 v[88:91], v[170:173], v[202:205], v[88:91]
	v_mfma_f32_16x16x32_bf16 v[84:87], v[178:181], v[202:205], v[84:87]
	v_mfma_f32_16x16x32_bf16 v[72:75], v[170:173], v[218:221], v[72:75]
	v_mfma_f32_16x16x32_bf16 v[68:71], v[178:181], v[218:221], v[68:71]
	s_setprio 0
	s_barrier
	s_add_i32 s21, s21, s52
	v_lshl_add_u64 v[162:163], v[162:163], 0, s[24:25]
	s_mov_b32 m0, s21
	ds_read_b128 v[182:185], v168 offset:49152
	ds_read_b128 v[186:189], v168 offset:50176
	ds_read_b128 v[190:193], v168 offset:51200
	ds_read_b128 v[194:197], v168 offset:52224
	ds_read_b128 v[198:201], v168 offset:53248
	ds_read_b128 v[202:205], v168 offset:54272
	ds_read_b128 v[206:209], v168 offset:55296
	ds_read_b128 v[218:221], v168 offset:56320
	global_load_lds_dwordx4 v[162:163], off
	v_lshl_add_u64 v[162:163], v[210:211], 0, s[24:25]
	s_add_i32 m0, s21, 0x2000
	s_add_i32 s21, s23, s52
	global_load_lds_dwordx4 v[162:163], off
	v_lshl_add_u64 v[162:163], v[212:213], 0, s[24:25]
	s_mov_b32 m0, s21
	s_nop 0
	global_load_lds_dwordx4 v[162:163], off
	v_lshl_add_u64 v[162:163], v[214:215], 0, s[24:25]
	s_add_i32 m0, s21, 0x2000
	s_nop 0
	global_load_lds_dwordx4 v[162:163], off
	v_lshl_add_u64 v[162:163], v[222:223], 0, s[24:25]
	s_mov_b32 m0, s61
	s_nop 0
	global_load_lds_dwordx4 v[162:163], off
	v_lshl_add_u64 v[162:163], v[224:225], 0, s[24:25]
	s_mov_b32 m0, s62
	s_nop 0
	global_load_lds_dwordx4 v[162:163], off
	s_waitcnt vmcnt(8)
	s_waitcnt lgkmcnt(0)
	s_barrier
	s_setprio 1
	s_waitcnt lgkmcnt(0)
	v_mfma_f32_16x16x32_bf16 v[64:67], v[132:135], v[182:185], v[64:67]
	v_mfma_f32_16x16x32_bf16 v[60:63], v[140:143], v[182:185], v[60:63]
	v_mfma_f32_16x16x32_bf16 v[48:51], v[132:135], v[190:193], v[48:51]
	v_mfma_f32_16x16x32_bf16 v[44:47], v[140:143], v[190:193], v[44:47]
	v_mfma_f32_16x16x32_bf16 v[32:35], v[132:135], v[198:201], v[32:35]
	v_mfma_f32_16x16x32_bf16 v[28:31], v[140:143], v[198:201], v[28:31]
	v_mfma_f32_16x16x32_bf16 v[16:19], v[132:135], v[206:209], v[16:19]
	v_mfma_f32_16x16x32_bf16 v[12:15], v[140:143], v[206:209], v[12:15]
	v_mfma_f32_16x16x32_bf16 v[64:67], v[136:139], v[186:189], v[64:67]
	v_mfma_f32_16x16x32_bf16 v[60:63], v[154:157], v[186:189], v[60:63]
	v_mfma_f32_16x16x32_bf16 v[48:51], v[136:139], v[194:197], v[48:51]
	v_mfma_f32_16x16x32_bf16 v[44:47], v[154:157], v[194:197], v[44:47]
	v_mfma_f32_16x16x32_bf16 v[32:35], v[136:139], v[202:205], v[32:35]
	v_mfma_f32_16x16x32_bf16 v[28:31], v[154:157], v[202:205], v[28:31]
	v_mfma_f32_16x16x32_bf16 v[16:19], v[136:139], v[218:221], v[16:19]
	v_mfma_f32_16x16x32_bf16 v[12:15], v[154:157], v[218:221], v[12:15]
	s_setprio 0
	s_setprio 1
	v_mfma_f32_16x16x32_bf16 v[56:59], v[158:161], v[182:185], v[56:59]
	v_mfma_f32_16x16x32_bf16 v[52:55], v[174:177], v[182:185], v[52:55]
	v_mfma_f32_16x16x32_bf16 v[40:43], v[158:161], v[190:193], v[40:43]
	v_mfma_f32_16x16x32_bf16 v[36:39], v[174:177], v[190:193], v[36:39]
	v_mfma_f32_16x16x32_bf16 v[24:27], v[158:161], v[198:201], v[24:27]
	v_mfma_f32_16x16x32_bf16 v[20:23], v[174:177], v[198:201], v[20:23]
	v_mfma_f32_16x16x32_bf16 v[8:11], v[158:161], v[206:209], v[8:11]
	v_mfma_f32_16x16x32_bf16 v[4:7], v[174:177], v[206:209], v[4:7]
	v_mfma_f32_16x16x32_bf16 v[56:59], v[170:173], v[186:189], v[56:59]
	v_mfma_f32_16x16x32_bf16 v[52:55], v[178:181], v[186:189], v[52:55]
	v_mfma_f32_16x16x32_bf16 v[40:43], v[170:173], v[194:197], v[40:43]
	v_mfma_f32_16x16x32_bf16 v[36:39], v[178:181], v[194:197], v[36:39]
	v_mfma_f32_16x16x32_bf16 v[24:27], v[170:173], v[202:205], v[24:27]
	v_mfma_f32_16x16x32_bf16 v[20:23], v[178:181], v[202:205], v[20:23]
	v_mfma_f32_16x16x32_bf16 v[8:11], v[170:173], v[218:221], v[8:11]
	v_mfma_f32_16x16x32_bf16 v[4:7], v[178:181], v[218:221], v[4:7]
	s_setprio 0
	s_barrier
	s_add_u32 s2, s2, 0x100
	s_addc_u32 s3, s3, 0
	s_add_u32 s19, s19, 0x100
	s_addc_u32 s20, s20, 0
	s_cmp_ge_i32 s22, s59
	s_mov_b32 s21, s22
	s_cbranch_scc1 .LBB0_1330

.LBB0_3265:
	s_andn2_b64 vcc, exec, s[14:15]
	s_cbranch_vccnz .LBB0_3268
	v_mov_b32_e32 v141, v3
	v_mov_b32_e32 v145, v3
	s_add_u32 s19, s26, 0x100
	s_addc_u32 s20, s27, 0
	v_lshl_add_u64 v[148:149], s[36:37], 0, v[140:141]
	v_lshl_add_u64 v[150:151], s[36:37], 0, v[144:145]
	s_mov_b32 s21, 0
	s_mov_b64 s[26:27], 0
	s_cmp_eq_u32 s56, s21
	s_cselect_b64 vcc, -1, 0
	s_add_i32 s21, s21, 2
	s_add_u32 s30, s26, 0x100
	s_addc_u32 s31, s27, 0
	s_and_b64 s[22:23], vcc, exec
	s_cselect_b32 s23, 0, s30
	s_cselect_b32 s22, 0, s31
	s_add_u32 s40, s2, s23
	s_addc_u32 s41, s3, s22
	s_add_u32 s28, s19, s26
	s_addc_u32 s29, s20, s27
	s_add_i32 s65, 0, 0x10000
	s_and_b64 s[22:23], vcc, exec
	v_add_u32_e32 v141, s65, v147
	s_cselect_b32 s23, s43, s29
	s_cselect_b32 s22, s42, s28
	s_add_i32 s28, 0, 0x14000
	ds_read_b128 v[158:161], v141
	ds_read_b128 v[162:165], v141 offset:1024
	ds_read_b128 v[166:169], v141 offset:2048
	ds_read_b128 v[170:173], v141 offset:3072
	v_add_u32_e32 v141, s28, v147
	ds_read_b128 v[174:177], v141
	ds_read_b128 v[178:181], v141 offset:1024
	ds_read_b128 v[182:185], v141 offset:2048
	ds_read_b128 v[186:189], v141 offset:3072
	v_cndmask_b32_e32 v2, v142, v157, vcc
	v_cndmask_b32_e32 v141, v140, v156, vcc
	v_cndmask_b32_e32 v210, v146, v154, vcc
	v_cndmask_b32_e32 v145, v144, v155, vcc
	v_lshl_add_u64 v[212:213], v[148:149], 0, s[26:27]
	s_add_i32 m0, s49, 0xc000
	ds_read_b128 v[190:193], v153
	ds_read_b128 v[194:197], v153 offset:1024
	ds_read_b128 v[198:201], v153 offset:2048
	ds_read_b128 v[202:205], v153 offset:3072
	ds_read_b128 v[206:209], v153 offset:4096
	ds_read_b128 v[218:221], v153 offset:5120
	ds_read_b128 v[222:225], v153 offset:6144
	ds_read_b128 v[226:229], v153 offset:7168
	global_load_lds_dwordx4 v[212:213], off
	v_lshl_add_u64 v[212:213], v[150:151], 0, s[26:27]
	s_add_i32 m0, s49, 0xe000
	s_nop 0
	global_load_lds_dwordx4 v[212:213], off
	s_waitcnt vmcnt(8)
	s_waitcnt lgkmcnt(0)
	s_barrier
	s_setprio 1
	s_waitcnt lgkmcnt(0)
	v_mfma_f32_16x16x32_bf16 v[124:127], v[158:161], v[190:193], 0
	v_mfma_f32_16x16x32_bf16 v[120:123], v[166:169], v[190:193], 0
	v_mfma_f32_16x16x32_bf16 v[112:115], v[158:161], v[198:201], 0
	v_mfma_f32_16x16x32_bf16 v[104:107], v[166:169], v[198:201], 0
	v_mfma_f32_16x16x32_bf16 v[96:99], v[158:161], v[206:209], 0
	v_mfma_f32_16x16x32_bf16 v[88:91], v[166:169], v[206:209], 0
	v_mfma_f32_16x16x32_bf16 v[80:83], v[158:161], v[222:225], 0
	v_mfma_f32_16x16x32_bf16 v[72:75], v[166:169], v[222:225], 0
	v_mfma_f32_16x16x32_bf16 v[124:127], v[162:165], v[194:197], v[124:127]
	v_mfma_f32_16x16x32_bf16 v[120:123], v[170:173], v[194:197], v[120:123]
	v_mfma_f32_16x16x32_bf16 v[112:115], v[162:165], v[202:205], v[112:115]
	v_mfma_f32_16x16x32_bf16 v[104:107], v[170:173], v[202:205], v[104:107]
	v_mfma_f32_16x16x32_bf16 v[96:99], v[162:165], v[218:221], v[96:99]
	v_mfma_f32_16x16x32_bf16 v[88:91], v[170:173], v[218:221], v[88:91]
	v_mfma_f32_16x16x32_bf16 v[80:83], v[162:165], v[226:229], v[80:83]
	v_mfma_f32_16x16x32_bf16 v[72:75], v[170:173], v[226:229], v[72:75]
	s_setprio 0
	s_setprio 1
	v_mfma_f32_16x16x32_bf16 v[128:131], v[174:177], v[190:193], 0
	v_mfma_f32_16x16x32_bf16 v[116:119], v[182:185], v[190:193], 0
	v_mfma_f32_16x16x32_bf16 v[108:111], v[174:177], v[198:201], 0
	v_mfma_f32_16x16x32_bf16 v[100:103], v[182:185], v[198:201], 0
	v_mfma_f32_16x16x32_bf16 v[92:95], v[174:177], v[206:209], 0
	v_mfma_f32_16x16x32_bf16 v[84:87], v[182:185], v[206:209], 0
	v_mfma_f32_16x16x32_bf16 v[76:79], v[174:177], v[222:225], 0
	v_mfma_f32_16x16x32_bf16 v[68:71], v[182:185], v[222:225], 0
	v_mfma_f32_16x16x32_bf16 v[128:131], v[178:181], v[194:197], v[128:131]
	v_mfma_f32_16x16x32_bf16 v[116:119], v[186:189], v[194:197], v[116:119]
	v_mfma_f32_16x16x32_bf16 v[108:111], v[178:181], v[202:205], v[108:111]
	v_mfma_f32_16x16x32_bf16 v[100:103], v[186:189], v[202:205], v[100:103]
	v_mfma_f32_16x16x32_bf16 v[92:95], v[178:181], v[218:221], v[92:95]
	v_mfma_f32_16x16x32_bf16 v[84:87], v[186:189], v[218:221], v[84:87]
	v_mfma_f32_16x16x32_bf16 v[76:79], v[178:181], v[226:229], v[76:79]
	v_mfma_f32_16x16x32_bf16 v[68:71], v[186:189], v[226:229], v[68:71]
	s_setprio 0
	s_barrier
	s_add_i32 s26, s65, s47
	v_lshl_add_u64 v[212:213], s[22:23], 0, v[138:139]
	s_mov_b32 m0, s26
	ds_read_b128 v[190:193], v153 offset:16384
	ds_read_b128 v[194:197], v153 offset:17408
	ds_read_b128 v[198:201], v153 offset:18432
	ds_read_b128 v[202:205], v153 offset:19456
	ds_read_b128 v[206:209], v153 offset:20480
	ds_read_b128 v[218:221], v153 offset:21504
	ds_read_b128 v[222:225], v153 offset:22528
	ds_read_b128 v[226:229], v153 offset:23552
	global_load_lds_dwordx4 v[212:213], off
	s_add_i32 m0, s26, 0x2000
	v_lshl_add_u64 v[214:215], s[22:23], 0, v[136:137]
	s_add_u32 s22, s22, s6
	s_addc_u32 s23, s23, s7
	s_add_i32 s26, s28, s47
	global_load_lds_dwordx4 v[214:215], off
	v_lshl_add_u64 v[230:231], s[22:23], 0, v[138:139]
	s_mov_b32 m0, s26
	v_lshl_add_u64 v[240:241], s[22:23], 0, v[136:137]
	global_load_lds_dwordx4 v[230:231], off
	s_add_i32 m0, s26, 0x2000
	v_mov_b32_e32 v211, v3
	global_load_lds_dwordx4 v[240:241], off
	s_mov_b32 m0, s49
	v_lshl_add_u64 v[242:243], s[40:41], 0, v[2:3]
	global_load_lds_dwordx4 v2, s[40:41]
	s_mov_b32 m0, s50
	s_nop 0
	global_load_lds_dwordx4 v210, s[40:41]
	s_waitcnt vmcnt(8)
	s_waitcnt lgkmcnt(0)
	v_lshl_add_u64 v[210:211], s[40:41], 0, v[210:211]
	s_barrier
	s_setprio 1
	s_waitcnt lgkmcnt(0)
	v_mfma_f32_16x16x32_bf16 v[64:67], v[158:161], v[190:193], 0
	v_mfma_f32_16x16x32_bf16 v[56:59], v[166:169], v[190:193], 0
	v_mfma_f32_16x16x32_bf16 v[48:51], v[158:161], v[198:201], 0
	v_mfma_f32_16x16x32_bf16 v[40:43], v[166:169], v[198:201], 0
	v_mfma_f32_16x16x32_bf16 v[32:35], v[158:161], v[206:209], 0
	v_mfma_f32_16x16x32_bf16 v[24:27], v[166:169], v[206:209], 0
	v_mfma_f32_16x16x32_bf16 v[16:19], v[158:161], v[222:225], 0
	v_mfma_f32_16x16x32_bf16 v[8:11], v[166:169], v[222:225], 0
	v_mfma_f32_16x16x32_bf16 v[64:67], v[162:165], v[194:197], v[64:67]
	v_mfma_f32_16x16x32_bf16 v[56:59], v[170:173], v[194:197], v[56:59]
	v_mfma_f32_16x16x32_bf16 v[48:51], v[162:165], v[202:205], v[48:51]
	v_mfma_f32_16x16x32_bf16 v[40:43], v[170:173], v[202:205], v[40:43]
	v_mfma_f32_16x16x32_bf16 v[32:35], v[162:165], v[218:221], v[32:35]
	v_mfma_f32_16x16x32_bf16 v[24:27], v[170:173], v[218:221], v[24:27]
	v_mfma_f32_16x16x32_bf16 v[16:19], v[162:165], v[226:229], v[16:19]
	v_mfma_f32_16x16x32_bf16 v[8:11], v[170:173], v[226:229], v[8:11]
	s_setprio 0
	s_setprio 1
	v_mfma_f32_16x16x32_bf16 v[60:63], v[174:177], v[190:193], 0
	v_mfma_f32_16x16x32_bf16 v[52:55], v[182:185], v[190:193], 0
	v_mfma_f32_16x16x32_bf16 v[44:47], v[174:177], v[198:201], 0
	v_mfma_f32_16x16x32_bf16 v[36:39], v[182:185], v[198:201], 0
	v_mfma_f32_16x16x32_bf16 v[28:31], v[174:177], v[206:209], 0
	v_mfma_f32_16x16x32_bf16 v[20:23], v[182:185], v[206:209], 0
	v_mfma_f32_16x16x32_bf16 v[12:15], v[174:177], v[222:225], 0
	v_mfma_f32_16x16x32_bf16 v[4:7], v[182:185], v[222:225], 0
	v_mfma_f32_16x16x32_bf16 v[60:63], v[178:181], v[194:197], v[60:63]
	v_mfma_f32_16x16x32_bf16 v[52:55], v[186:189], v[194:197], v[52:55]
	v_mfma_f32_16x16x32_bf16 v[44:47], v[178:181], v[202:205], v[44:47]
	v_mfma_f32_16x16x32_bf16 v[36:39], v[186:189], v[202:205], v[36:39]
	v_mfma_f32_16x16x32_bf16 v[28:31], v[178:181], v[218:221], v[28:31]
	v_mfma_f32_16x16x32_bf16 v[20:23], v[186:189], v[218:221], v[20:23]
	v_mfma_f32_16x16x32_bf16 v[12:15], v[178:181], v[226:229], v[12:15]
	v_mfma_f32_16x16x32_bf16 v[4:7], v[186:189], v[226:229], v[4:7]
	s_setprio 0
	s_barrier
	s_add_i32 s22, 0, 0x18000
	v_add_u32_e32 v2, s22, v147
	s_add_i32 s23, 0, 0x1c000
	ds_read_b128 v[158:161], v2
	ds_read_b128 v[162:165], v2 offset:1024
	ds_read_b128 v[166:169], v2 offset:2048
	ds_read_b128 v[170:173], v2 offset:3072
	v_add_u32_e32 v2, s23, v147
	ds_read_b128 v[174:177], v2
	ds_read_b128 v[178:181], v2 offset:1024
	ds_read_b128 v[182:185], v2 offset:2048
	ds_read_b128 v[186:189], v2 offset:3072
	s_mov_b32 m0, s51
	ds_read_b128 v[190:193], v153 offset:32768
	ds_read_b128 v[194:197], v153 offset:33792
	ds_read_b128 v[198:201], v153 offset:34816
	ds_read_b128 v[202:205], v153 offset:35840
	ds_read_b128 v[206:209], v153 offset:36864
	ds_read_b128 v[218:221], v153 offset:37888
	ds_read_b128 v[222:225], v153 offset:38912
	ds_read_b128 v[226:229], v153 offset:39936
	global_load_lds_dwordx4 v141, s[40:41]
	s_mov_b32 m0, s52
	s_nop 0
	global_load_lds_dwordx4 v145, s[40:41]
	s_waitcnt vmcnt(8)
	s_waitcnt lgkmcnt(0)
	s_barrier
	s_setprio 1
	s_waitcnt lgkmcnt(0)
	v_mfma_f32_16x16x32_bf16 v[124:127], v[158:161], v[190:193], v[124:127]
	v_mfma_f32_16x16x32_bf16 v[120:123], v[166:169], v[190:193], v[120:123]
	v_mfma_f32_16x16x32_bf16 v[112:115], v[158:161], v[198:201], v[112:115]
	v_mfma_f32_16x16x32_bf16 v[104:107], v[166:169], v[198:201], v[104:107]
	v_mfma_f32_16x16x32_bf16 v[96:99], v[158:161], v[206:209], v[96:99]
	v_mfma_f32_16x16x32_bf16 v[88:91], v[166:169], v[206:209], v[88:91]
	v_mfma_f32_16x16x32_bf16 v[80:83], v[158:161], v[222:225], v[80:83]
	v_mfma_f32_16x16x32_bf16 v[72:75], v[166:169], v[222:225], v[72:75]
	v_mfma_f32_16x16x32_bf16 v[124:127], v[162:165], v[194:197], v[124:127]
	v_mfma_f32_16x16x32_bf16 v[120:123], v[170:173], v[194:197], v[120:123]
	v_mfma_f32_16x16x32_bf16 v[112:115], v[162:165], v[202:205], v[112:115]
	v_mfma_f32_16x16x32_bf16 v[104:107], v[170:173], v[202:205], v[104:107]
	v_mfma_f32_16x16x32_bf16 v[96:99], v[162:165], v[218:221], v[96:99]
	v_mfma_f32_16x16x32_bf16 v[88:91], v[170:173], v[218:221], v[88:91]
	v_mfma_f32_16x16x32_bf16 v[80:83], v[162:165], v[226:229], v[80:83]
	v_mfma_f32_16x16x32_bf16 v[72:75], v[170:173], v[226:229], v[72:75]
	s_setprio 0
	s_setprio 1
	v_mfma_f32_16x16x32_bf16 v[128:131], v[174:177], v[190:193], v[128:131]
	v_mfma_f32_16x16x32_bf16 v[116:119], v[182:185], v[190:193], v[116:119]
	v_mfma_f32_16x16x32_bf16 v[108:111], v[174:177], v[198:201], v[108:111]
	v_mfma_f32_16x16x32_bf16 v[100:103], v[182:185], v[198:201], v[100:103]
	v_mfma_f32_16x16x32_bf16 v[92:95], v[174:177], v[206:209], v[92:95]
	v_mfma_f32_16x16x32_bf16 v[84:87], v[182:185], v[206:209], v[84:87]
	v_mfma_f32_16x16x32_bf16 v[76:79], v[174:177], v[222:225], v[76:79]
	v_mfma_f32_16x16x32_bf16 v[68:71], v[182:185], v[222:225], v[68:71]
	v_mfma_f32_16x16x32_bf16 v[128:131], v[178:181], v[194:197], v[128:131]
	v_mfma_f32_16x16x32_bf16 v[116:119], v[186:189], v[194:197], v[116:119]
	v_mfma_f32_16x16x32_bf16 v[108:111], v[178:181], v[202:205], v[108:111]
	v_mfma_f32_16x16x32_bf16 v[100:103], v[186:189], v[202:205], v[100:103]
	v_mfma_f32_16x16x32_bf16 v[92:95], v[178:181], v[218:221], v[92:95]
	v_mfma_f32_16x16x32_bf16 v[84:87], v[186:189], v[218:221], v[84:87]
	v_mfma_f32_16x16x32_bf16 v[76:79], v[178:181], v[226:229], v[76:79]
	v_mfma_f32_16x16x32_bf16 v[68:71], v[186:189], v[226:229], v[68:71]
	s_setprio 0
	s_barrier
	s_add_i32 s22, s22, s47
	v_lshl_add_u64 v[212:213], v[212:213], 0, s[24:25]
	s_mov_b32 m0, s22
	ds_read_b128 v[190:193], v153 offset:49152
	ds_read_b128 v[194:197], v153 offset:50176
	ds_read_b128 v[198:201], v153 offset:51200
	ds_read_b128 v[202:205], v153 offset:52224
	ds_read_b128 v[206:209], v153 offset:53248
	ds_read_b128 v[218:221], v153 offset:54272
	ds_read_b128 v[222:225], v153 offset:55296
	ds_read_b128 v[226:229], v153 offset:56320
	global_load_lds_dwordx4 v[212:213], off
	v_lshl_add_u64 v[212:213], v[214:215], 0, s[24:25]
	s_add_i32 m0, s22, 0x2000
	s_add_i32 s22, s23, s47
	global_load_lds_dwordx4 v[212:213], off
	v_lshl_add_u64 v[212:213], v[230:231], 0, s[24:25]
	s_mov_b32 m0, s22
	v_lshl_add_u64 v[210:211], v[210:211], 0, s[24:25]
	global_load_lds_dwordx4 v[212:213], off
	v_lshl_add_u64 v[212:213], v[240:241], 0, s[24:25]
	s_add_i32 m0, s22, 0x2000
	s_nop 0
	global_load_lds_dwordx4 v[212:213], off
	v_lshl_add_u64 v[212:213], v[242:243], 0, s[24:25]
	s_mov_b32 m0, s53
	s_nop 0
	global_load_lds_dwordx4 v[212:213], off
	s_mov_b32 m0, s54
	s_nop 0
	global_load_lds_dwordx4 v[210:211], off
	s_waitcnt vmcnt(8)
	s_waitcnt lgkmcnt(0)
	s_barrier
	s_setprio 1
	s_waitcnt lgkmcnt(0)
	v_mfma_f32_16x16x32_bf16 v[64:67], v[158:161], v[190:193], v[64:67]
	v_mfma_f32_16x16x32_bf16 v[56:59], v[166:169], v[190:193], v[56:59]
	v_mfma_f32_16x16x32_bf16 v[48:51], v[158:161], v[198:201], v[48:51]
	v_mfma_f32_16x16x32_bf16 v[40:43], v[166:169], v[198:201], v[40:43]
	v_mfma_f32_16x16x32_bf16 v[32:35], v[158:161], v[206:209], v[32:35]
	v_mfma_f32_16x16x32_bf16 v[24:27], v[166:169], v[206:209], v[24:27]
	v_mfma_f32_16x16x32_bf16 v[16:19], v[158:161], v[222:225], v[16:19]
	v_mfma_f32_16x16x32_bf16 v[8:11], v[166:169], v[222:225], v[8:11]
	v_mfma_f32_16x16x32_bf16 v[64:67], v[162:165], v[194:197], v[64:67]
	v_mfma_f32_16x16x32_bf16 v[56:59], v[170:173], v[194:197], v[56:59]
	v_mfma_f32_16x16x32_bf16 v[48:51], v[162:165], v[202:205], v[48:51]
	v_mfma_f32_16x16x32_bf16 v[40:43], v[170:173], v[202:205], v[40:43]
	v_mfma_f32_16x16x32_bf16 v[32:35], v[162:165], v[218:221], v[32:35]
	v_mfma_f32_16x16x32_bf16 v[24:27], v[170:173], v[218:221], v[24:27]
	v_mfma_f32_16x16x32_bf16 v[16:19], v[162:165], v[226:229], v[16:19]
	v_mfma_f32_16x16x32_bf16 v[8:11], v[170:173], v[226:229], v[8:11]
	s_setprio 0
	s_setprio 1
	v_mfma_f32_16x16x32_bf16 v[60:63], v[174:177], v[190:193], v[60:63]
	v_mfma_f32_16x16x32_bf16 v[52:55], v[182:185], v[190:193], v[52:55]
	v_mfma_f32_16x16x32_bf16 v[44:47], v[174:177], v[198:201], v[44:47]
	v_mfma_f32_16x16x32_bf16 v[36:39], v[182:185], v[198:201], v[36:39]
	v_mfma_f32_16x16x32_bf16 v[28:31], v[174:177], v[206:209], v[28:31]
	v_mfma_f32_16x16x32_bf16 v[20:23], v[182:185], v[206:209], v[20:23]
	v_mfma_f32_16x16x32_bf16 v[12:15], v[174:177], v[222:225], v[12:15]
	v_mfma_f32_16x16x32_bf16 v[4:7], v[182:185], v[222:225], v[4:7]
	v_mfma_f32_16x16x32_bf16 v[60:63], v[178:181], v[194:197], v[60:63]
	v_mfma_f32_16x16x32_bf16 v[52:55], v[186:189], v[194:197], v[52:55]
	v_mfma_f32_16x16x32_bf16 v[44:47], v[178:181], v[202:205], v[44:47]
	v_mfma_f32_16x16x32_bf16 v[36:39], v[186:189], v[202:205], v[36:39]
	v_mfma_f32_16x16x32_bf16 v[28:31], v[178:181], v[218:221], v[28:31]
	v_mfma_f32_16x16x32_bf16 v[20:23], v[186:189], v[218:221], v[20:23]
	v_mfma_f32_16x16x32_bf16 v[12:15], v[178:181], v[226:229], v[12:15]
	v_mfma_f32_16x16x32_bf16 v[4:7], v[186:189], v[226:229], v[4:7]
	s_setprio 0
	s_barrier
	s_cmp_ge_i32 s21, s55
	s_mov_b64 s[26:27], s[30:31]
	s_cbranch_scc1 .LBB0_3268

.LBB0_3497:
	s_andn2_b64 vcc, exec, s[10:11]
	s_cbranch_vccnz .LBB0_3500
	s_add_u32 s26, s26, 0x80
	s_addc_u32 s27, s27, 0
	s_add_u32 s19, s30, 0x100
	s_addc_u32 s20, s31, 0
	s_mov_b32 s21, 0
	s_add_i32 s22, s21, 2
	s_add_u32 s23, s26, 0x80
	s_addc_u32 s28, s27, 0
	s_add_i32 s55, 0, 0x10000
	s_cmp_eq_u32 s49, s21
	s_cselect_b32 s31, s15, s28
	s_cselect_b32 s30, s14, s23
	v_add_u32_e32 v2, s55, v145
	s_cselect_b32 s29, s17, s20
	s_cselect_b32 s28, s16, s19
	s_add_i32 s21, 0, 0x14000
	ds_read_b128 v[148:151], v2
	ds_read_b128 v[152:155], v2 offset:1024
	ds_read_b128 v[156:159], v2 offset:2048
	ds_read_b128 v[160:163], v2 offset:3072
	v_add_u32_e32 v2, s21, v145
	ds_read_b128 v[164:167], v2
	ds_read_b128 v[168:171], v2 offset:1024
	ds_read_b128 v[172:175], v2 offset:2048
	ds_read_b128 v[176:179], v2 offset:3072
	v_lshl_add_u64 v[212:213], s[26:27], 0, v[140:141]
	s_add_i32 m0, s42, 0xc000
	ds_read_b128 v[180:183], v147
	ds_read_b128 v[184:187], v147 offset:1024
	ds_read_b128 v[188:191], v147 offset:2048
	ds_read_b128 v[192:195], v147 offset:3072
	ds_read_b128 v[196:199], v147 offset:4096
	ds_read_b128 v[200:203], v147 offset:5120
	ds_read_b128 v[204:207], v147 offset:6144
	ds_read_b128 v[208:211], v147 offset:7168
	global_load_lds_dwordx4 v[212:213], off
	v_lshl_add_u64 v[212:213], s[26:27], 0, v[142:143]
	s_add_i32 m0, s42, 0xe000
	s_nop 0
	global_load_lds_dwordx4 v[212:213], off
	s_waitcnt vmcnt(8)
	s_waitcnt lgkmcnt(0)
	s_barrier
	s_setprio 1
	s_waitcnt lgkmcnt(0)
	v_mfma_f32_16x16x32_bf16 v[124:127], v[148:151], v[180:183], 0
	v_mfma_f32_16x16x32_bf16 v[128:131], v[156:159], v[180:183], 0
	v_mfma_f32_16x16x32_bf16 v[112:115], v[148:151], v[188:191], 0
	v_mfma_f32_16x16x32_bf16 v[108:111], v[156:159], v[188:191], 0
	v_mfma_f32_16x16x32_bf16 v[96:99], v[148:151], v[196:199], 0
	v_mfma_f32_16x16x32_bf16 v[92:95], v[156:159], v[196:199], 0
	v_mfma_f32_16x16x32_bf16 v[80:83], v[148:151], v[204:207], 0
	v_mfma_f32_16x16x32_bf16 v[76:79], v[156:159], v[204:207], 0
	v_mfma_f32_16x16x32_bf16 v[124:127], v[152:155], v[184:187], v[124:127]
	v_mfma_f32_16x16x32_bf16 v[128:131], v[160:163], v[184:187], v[128:131]
	v_mfma_f32_16x16x32_bf16 v[112:115], v[152:155], v[192:195], v[112:115]
	v_mfma_f32_16x16x32_bf16 v[108:111], v[160:163], v[192:195], v[108:111]
	v_mfma_f32_16x16x32_bf16 v[96:99], v[152:155], v[200:203], v[96:99]
	v_mfma_f32_16x16x32_bf16 v[92:95], v[160:163], v[200:203], v[92:95]
	v_mfma_f32_16x16x32_bf16 v[80:83], v[152:155], v[208:211], v[80:83]
	v_mfma_f32_16x16x32_bf16 v[76:79], v[160:163], v[208:211], v[76:79]
	s_setprio 0
	s_setprio 1
	v_mfma_f32_16x16x32_bf16 v[120:123], v[164:167], v[180:183], 0
	v_mfma_f32_16x16x32_bf16 v[116:119], v[172:175], v[180:183], 0
	v_mfma_f32_16x16x32_bf16 v[104:107], v[164:167], v[188:191], 0
	v_mfma_f32_16x16x32_bf16 v[100:103], v[172:175], v[188:191], 0
	v_mfma_f32_16x16x32_bf16 v[88:91], v[164:167], v[196:199], 0
	v_mfma_f32_16x16x32_bf16 v[84:87], v[172:175], v[196:199], 0
	v_mfma_f32_16x16x32_bf16 v[72:75], v[164:167], v[204:207], 0
	v_mfma_f32_16x16x32_bf16 v[68:71], v[172:175], v[204:207], 0
	v_mfma_f32_16x16x32_bf16 v[120:123], v[168:171], v[184:187], v[120:123]
	v_mfma_f32_16x16x32_bf16 v[116:119], v[176:179], v[184:187], v[116:119]
	v_mfma_f32_16x16x32_bf16 v[104:107], v[168:171], v[192:195], v[104:107]
	v_mfma_f32_16x16x32_bf16 v[100:103], v[176:179], v[192:195], v[100:103]
	v_mfma_f32_16x16x32_bf16 v[88:91], v[168:171], v[200:203], v[88:91]
	v_mfma_f32_16x16x32_bf16 v[84:87], v[176:179], v[200:203], v[84:87]
	v_mfma_f32_16x16x32_bf16 v[72:75], v[168:171], v[208:211], v[72:75]
	v_mfma_f32_16x16x32_bf16 v[68:71], v[176:179], v[208:211], v[68:71]
	s_setprio 0
	s_barrier
	s_add_i32 s23, s55, s41
	v_lshl_add_u64 v[212:213], s[28:29], 0, v[136:137]
	s_mov_b32 m0, s23
	ds_read_b128 v[180:183], v147 offset:16384
	ds_read_b128 v[184:187], v147 offset:17408
	ds_read_b128 v[188:191], v147 offset:18432
	ds_read_b128 v[192:195], v147 offset:19456
	ds_read_b128 v[196:199], v147 offset:20480
	ds_read_b128 v[200:203], v147 offset:21504
	ds_read_b128 v[204:207], v147 offset:22528
	ds_read_b128 v[208:211], v147 offset:23552
	global_load_lds_dwordx4 v[212:213], off
	s_add_i32 m0, s23, 0x2000
	v_lshl_add_u64 v[214:215], s[28:29], 0, v[132:133]
	s_add_u32 s28, s28, s2
	s_addc_u32 s29, s29, s3
	s_add_i32 s21, s21, s41
	global_load_lds_dwordx4 v[214:215], off
	v_lshl_add_u64 v[218:219], s[28:29], 0, v[136:137]
	s_mov_b32 m0, s21
	v_lshl_add_u64 v[220:221], s[28:29], 0, v[132:133]
	global_load_lds_dwordx4 v[218:219], off
	s_add_i32 m0, s21, 0x2000
	v_lshl_add_u64 v[222:223], s[30:31], 0, v[138:139]
	global_load_lds_dwordx4 v[220:221], off
	s_mov_b32 m0, s42
	v_lshl_add_u64 v[224:225], s[30:31], 0, v[134:135]
	global_load_lds_dwordx4 v[222:223], off
	s_mov_b32 m0, s43
	s_nop 0
	global_load_lds_dwordx4 v[224:225], off
	s_waitcnt vmcnt(8)
	s_waitcnt lgkmcnt(0)
	s_barrier
	s_setprio 1
	s_waitcnt lgkmcnt(0)
	v_mfma_f32_16x16x32_bf16 v[64:67], v[148:151], v[180:183], 0
	v_mfma_f32_16x16x32_bf16 v[60:63], v[156:159], v[180:183], 0
	v_mfma_f32_16x16x32_bf16 v[48:51], v[148:151], v[188:191], 0
	v_mfma_f32_16x16x32_bf16 v[44:47], v[156:159], v[188:191], 0
	v_mfma_f32_16x16x32_bf16 v[32:35], v[148:151], v[196:199], 0
	v_mfma_f32_16x16x32_bf16 v[28:31], v[156:159], v[196:199], 0
	v_mfma_f32_16x16x32_bf16 v[16:19], v[148:151], v[204:207], 0
	v_mfma_f32_16x16x32_bf16 v[12:15], v[156:159], v[204:207], 0
	v_mfma_f32_16x16x32_bf16 v[64:67], v[152:155], v[184:187], v[64:67]
	v_mfma_f32_16x16x32_bf16 v[60:63], v[160:163], v[184:187], v[60:63]
	v_mfma_f32_16x16x32_bf16 v[48:51], v[152:155], v[192:195], v[48:51]
	v_mfma_f32_16x16x32_bf16 v[44:47], v[160:163], v[192:195], v[44:47]
	v_mfma_f32_16x16x32_bf16 v[32:35], v[152:155], v[200:203], v[32:35]
	v_mfma_f32_16x16x32_bf16 v[28:31], v[160:163], v[200:203], v[28:31]
	v_mfma_f32_16x16x32_bf16 v[16:19], v[152:155], v[208:211], v[16:19]
	v_mfma_f32_16x16x32_bf16 v[12:15], v[160:163], v[208:211], v[12:15]
	s_setprio 0
	s_setprio 1
	v_mfma_f32_16x16x32_bf16 v[56:59], v[164:167], v[180:183], 0
	v_mfma_f32_16x16x32_bf16 v[52:55], v[172:175], v[180:183], 0
	v_mfma_f32_16x16x32_bf16 v[40:43], v[164:167], v[188:191], 0
	v_mfma_f32_16x16x32_bf16 v[36:39], v[172:175], v[188:191], 0
	v_mfma_f32_16x16x32_bf16 v[24:27], v[164:167], v[196:199], 0
	v_mfma_f32_16x16x32_bf16 v[20:23], v[172:175], v[196:199], 0
	v_mfma_f32_16x16x32_bf16 v[8:11], v[164:167], v[204:207], 0
	v_mfma_f32_16x16x32_bf16 v[4:7], v[172:175], v[204:207], 0
	v_mfma_f32_16x16x32_bf16 v[56:59], v[168:171], v[184:187], v[56:59]
	v_mfma_f32_16x16x32_bf16 v[52:55], v[176:179], v[184:187], v[52:55]
	v_mfma_f32_16x16x32_bf16 v[40:43], v[168:171], v[192:195], v[40:43]
	v_mfma_f32_16x16x32_bf16 v[36:39], v[176:179], v[192:195], v[36:39]
	v_mfma_f32_16x16x32_bf16 v[24:27], v[168:171], v[200:203], v[24:27]
	v_mfma_f32_16x16x32_bf16 v[20:23], v[176:179], v[200:203], v[20:23]
	v_mfma_f32_16x16x32_bf16 v[8:11], v[168:171], v[208:211], v[8:11]
	v_mfma_f32_16x16x32_bf16 v[4:7], v[176:179], v[208:211], v[4:7]
	s_setprio 0
	s_barrier
	s_add_i32 s21, 0, 0x18000
	v_add_u32_e32 v2, s21, v145
	s_add_i32 s23, 0, 0x1c000
	ds_read_b128 v[148:151], v2
	ds_read_b128 v[152:155], v2 offset:1024
	ds_read_b128 v[156:159], v2 offset:2048
	ds_read_b128 v[160:163], v2 offset:3072
	v_add_u32_e32 v2, s23, v145
	ds_read_b128 v[164:167], v2
	ds_read_b128 v[168:171], v2 offset:1024
	ds_read_b128 v[172:175], v2 offset:2048
	ds_read_b128 v[176:179], v2 offset:3072
	s_add_u32 s28, s30, s2
	s_addc_u32 s29, s31, s3
	s_mov_b32 m0, s44
	v_lshl_add_u64 v[226:227], s[28:29], 0, v[138:139]
	ds_read_b128 v[180:183], v147 offset:32768
	ds_read_b128 v[184:187], v147 offset:33792
	ds_read_b128 v[188:191], v147 offset:34816
	ds_read_b128 v[192:195], v147 offset:35840
	ds_read_b128 v[196:199], v147 offset:36864
	ds_read_b128 v[200:203], v147 offset:37888
	ds_read_b128 v[204:207], v147 offset:38912
	ds_read_b128 v[208:211], v147 offset:39936
	global_load_lds_dwordx4 v[226:227], off
	v_lshl_add_u64 v[226:227], s[28:29], 0, v[134:135]
	s_mov_b32 m0, s45
	s_nop 0
	global_load_lds_dwordx4 v[226:227], off
	s_waitcnt vmcnt(8)
	s_waitcnt lgkmcnt(0)
	s_barrier
	s_setprio 1
	s_waitcnt lgkmcnt(0)
	v_mfma_f32_16x16x32_bf16 v[124:127], v[148:151], v[180:183], v[124:127]
	v_mfma_f32_16x16x32_bf16 v[128:131], v[156:159], v[180:183], v[128:131]
	v_mfma_f32_16x16x32_bf16 v[112:115], v[148:151], v[188:191], v[112:115]
	v_mfma_f32_16x16x32_bf16 v[108:111], v[156:159], v[188:191], v[108:111]
	v_mfma_f32_16x16x32_bf16 v[96:99], v[148:151], v[196:199], v[96:99]
	v_mfma_f32_16x16x32_bf16 v[92:95], v[156:159], v[196:199], v[92:95]
	v_mfma_f32_16x16x32_bf16 v[80:83], v[148:151], v[204:207], v[80:83]
	v_mfma_f32_16x16x32_bf16 v[76:79], v[156:159], v[204:207], v[76:79]
	v_mfma_f32_16x16x32_bf16 v[124:127], v[152:155], v[184:187], v[124:127]
	v_mfma_f32_16x16x32_bf16 v[128:131], v[160:163], v[184:187], v[128:131]
	v_mfma_f32_16x16x32_bf16 v[112:115], v[152:155], v[192:195], v[112:115]
	v_mfma_f32_16x16x32_bf16 v[108:111], v[160:163], v[192:195], v[108:111]
	v_mfma_f32_16x16x32_bf16 v[96:99], v[152:155], v[200:203], v[96:99]
	v_mfma_f32_16x16x32_bf16 v[92:95], v[160:163], v[200:203], v[92:95]
	v_mfma_f32_16x16x32_bf16 v[80:83], v[152:155], v[208:211], v[80:83]
	v_mfma_f32_16x16x32_bf16 v[76:79], v[160:163], v[208:211], v[76:79]
	s_setprio 0
	s_setprio 1
	v_mfma_f32_16x16x32_bf16 v[120:123], v[164:167], v[180:183], v[120:123]
	v_mfma_f32_16x16x32_bf16 v[116:119], v[172:175], v[180:183], v[116:119]
	v_mfma_f32_16x16x32_bf16 v[104:107], v[164:167], v[188:191], v[104:107]
	v_mfma_f32_16x16x32_bf16 v[100:103], v[172:175], v[188:191], v[100:103]
	v_mfma_f32_16x16x32_bf16 v[88:91], v[164:167], v[196:199], v[88:91]
	v_mfma_f32_16x16x32_bf16 v[84:87], v[172:175], v[196:199], v[84:87]
	v_mfma_f32_16x16x32_bf16 v[72:75], v[164:167], v[204:207], v[72:75]
	v_mfma_f32_16x16x32_bf16 v[68:71], v[172:175], v[204:207], v[68:71]
	v_mfma_f32_16x16x32_bf16 v[120:123], v[168:171], v[184:187], v[120:123]
	v_mfma_f32_16x16x32_bf16 v[116:119], v[176:179], v[184:187], v[116:119]
	v_mfma_f32_16x16x32_bf16 v[104:107], v[168:171], v[192:195], v[104:107]
	v_mfma_f32_16x16x32_bf16 v[100:103], v[176:179], v[192:195], v[100:103]
	v_mfma_f32_16x16x32_bf16 v[88:91], v[168:171], v[200:203], v[88:91]
	v_mfma_f32_16x16x32_bf16 v[84:87], v[176:179], v[200:203], v[84:87]
	v_mfma_f32_16x16x32_bf16 v[72:75], v[168:171], v[208:211], v[72:75]
	v_mfma_f32_16x16x32_bf16 v[68:71], v[176:179], v[208:211], v[68:71]
	s_setprio 0
	s_barrier
	s_add_i32 s21, s21, s41
	v_lshl_add_u64 v[212:213], v[212:213], 0, s[24:25]
	s_mov_b32 m0, s21
	ds_read_b128 v[180:183], v147 offset:49152
	ds_read_b128 v[184:187], v147 offset:50176
	ds_read_b128 v[188:191], v147 offset:51200
	ds_read_b128 v[192:195], v147 offset:52224
	ds_read_b128 v[196:199], v147 offset:53248
	ds_read_b128 v[200:203], v147 offset:54272
	ds_read_b128 v[204:207], v147 offset:55296
	ds_read_b128 v[208:211], v147 offset:56320
	global_load_lds_dwordx4 v[212:213], off
	v_lshl_add_u64 v[212:213], v[214:215], 0, s[24:25]
	s_add_i32 m0, s21, 0x2000
	s_add_i32 s21, s23, s41
	global_load_lds_dwordx4 v[212:213], off
	v_lshl_add_u64 v[212:213], v[218:219], 0, s[24:25]
	s_mov_b32 m0, s21
	s_nop 0
	global_load_lds_dwordx4 v[212:213], off
	v_lshl_add_u64 v[212:213], v[220:221], 0, s[24:25]
	s_add_i32 m0, s21, 0x2000
	s_nop 0
	global_load_lds_dwordx4 v[212:213], off
	v_lshl_add_u64 v[212:213], v[222:223], 0, s[24:25]
	s_mov_b32 m0, s47
	s_nop 0
	global_load_lds_dwordx4 v[212:213], off
	v_lshl_add_u64 v[212:213], v[224:225], 0, s[24:25]
	s_mov_b32 m0, s48
	s_nop 0
	global_load_lds_dwordx4 v[212:213], off
	s_waitcnt vmcnt(8)
	s_waitcnt lgkmcnt(0)
	s_barrier
	s_setprio 1
	s_waitcnt lgkmcnt(0)
	v_mfma_f32_16x16x32_bf16 v[64:67], v[148:151], v[180:183], v[64:67]
	v_mfma_f32_16x16x32_bf16 v[60:63], v[156:159], v[180:183], v[60:63]
	v_mfma_f32_16x16x32_bf16 v[48:51], v[148:151], v[188:191], v[48:51]
	v_mfma_f32_16x16x32_bf16 v[44:47], v[156:159], v[188:191], v[44:47]
	v_mfma_f32_16x16x32_bf16 v[32:35], v[148:151], v[196:199], v[32:35]
	v_mfma_f32_16x16x32_bf16 v[28:31], v[156:159], v[196:199], v[28:31]
	v_mfma_f32_16x16x32_bf16 v[16:19], v[148:151], v[204:207], v[16:19]
	v_mfma_f32_16x16x32_bf16 v[12:15], v[156:159], v[204:207], v[12:15]
	v_mfma_f32_16x16x32_bf16 v[64:67], v[152:155], v[184:187], v[64:67]
	v_mfma_f32_16x16x32_bf16 v[60:63], v[160:163], v[184:187], v[60:63]
	v_mfma_f32_16x16x32_bf16 v[48:51], v[152:155], v[192:195], v[48:51]
	v_mfma_f32_16x16x32_bf16 v[44:47], v[160:163], v[192:195], v[44:47]
	v_mfma_f32_16x16x32_bf16 v[32:35], v[152:155], v[200:203], v[32:35]
	v_mfma_f32_16x16x32_bf16 v[28:31], v[160:163], v[200:203], v[28:31]
	v_mfma_f32_16x16x32_bf16 v[16:19], v[152:155], v[208:211], v[16:19]
	v_mfma_f32_16x16x32_bf16 v[12:15], v[160:163], v[208:211], v[12:15]
	s_setprio 0
	s_setprio 1
	v_mfma_f32_16x16x32_bf16 v[56:59], v[164:167], v[180:183], v[56:59]
	v_mfma_f32_16x16x32_bf16 v[52:55], v[172:175], v[180:183], v[52:55]
	v_mfma_f32_16x16x32_bf16 v[40:43], v[164:167], v[188:191], v[40:43]
	v_mfma_f32_16x16x32_bf16 v[36:39], v[172:175], v[188:191], v[36:39]
	v_mfma_f32_16x16x32_bf16 v[24:27], v[164:167], v[196:199], v[24:27]
	v_mfma_f32_16x16x32_bf16 v[20:23], v[172:175], v[196:199], v[20:23]
	v_mfma_f32_16x16x32_bf16 v[8:11], v[164:167], v[204:207], v[8:11]
	v_mfma_f32_16x16x32_bf16 v[4:7], v[172:175], v[204:207], v[4:7]
	v_mfma_f32_16x16x32_bf16 v[56:59], v[168:171], v[184:187], v[56:59]
	v_mfma_f32_16x16x32_bf16 v[52:55], v[176:179], v[184:187], v[52:55]
	v_mfma_f32_16x16x32_bf16 v[40:43], v[168:171], v[192:195], v[40:43]
	v_mfma_f32_16x16x32_bf16 v[36:39], v[176:179], v[192:195], v[36:39]
	v_mfma_f32_16x16x32_bf16 v[24:27], v[168:171], v[200:203], v[24:27]
	v_mfma_f32_16x16x32_bf16 v[20:23], v[176:179], v[200:203], v[20:23]
	v_mfma_f32_16x16x32_bf16 v[8:11], v[168:171], v[208:211], v[8:11]
	v_mfma_f32_16x16x32_bf16 v[4:7], v[176:179], v[208:211], v[4:7]
	s_setprio 0
	s_barrier
	s_add_u32 s26, s26, 0x100
	s_addc_u32 s27, s27, 0
	s_add_u32 s19, s19, 0x100
	s_addc_u32 s20, s20, 0
	s_cmp_ge_i32 s22, s46
	s_mov_b32 s21, s22
	s_cbranch_scc1 .LBB0_3500
